# attention overflow-test chains: dropped the canonicalizing v_max x,x in front of the cross-half v_max (13 sites)
# baseline (speedup 1.0000x reference)
; #define GAS __attribute__((address_space(1)))
; #define LAS __attribute__((address_space(3)))
; __device__ __forceinline__ void swa_phase(const Ctx& C, const bf16* PROJ, const float* sinks, bf16* YSWA) {
;     ...
;         for (int i = 0; i < 2; ++i) { const int task = C.tid + 512 * i, kk = 2 * (task >> 3), c8 = task & 7;
;             v4u va = {0u, 0u, 0u, 0u}, vb = {0u, 0u, 0u, 0u};
;             if (n > 0 || kk >= 128) { const bf16* vp = PROJ + (size_t)(tb - 128 + kk) * INW + C_VS + 64 * hk + 8 * c8; va = *(const GAS v4u*)vp; vb = *(const GAS v4u*)(vp + INW); }
;             LAS unsigned* dst = (LAS unsigned*)(vt + (8 * c8) * 264 + kk);
;             dst[0] = (va.x & 0xffffu) | (vb.x << 16); dst[132] = (va.x >> 16) | (vb.x & 0xffff0000u); dst[2 * 132] = (va.y & 0xffffu) | (vb.y << 16); dst[3 * 132] = (va.y >> 16) | (vb.y & 0xffff0000u);
;             dst[4 * 132] = (va.z & 0xffffu) | (vb.z << 16); dst[5 * 132] = (va.z >> 16) | (vb.z & 0xffff0000u); dst[6 * 132] = (va.w & 0xffffu) | (vb.w << 16); dst[7 * 132] = (va.w >> 16) | (vb.w & 0xffff0000u); }
;         bf16x8 kf[9][2], qf[3][2];
;         { const int q0_ = tb + 16 * w;
; #pragma unroll
;           for (int j = 0; j < 9; ++j) { const int krow = 16 * w - 128 + 16 * j + c16; int ktok = tb + krow; if (128 * n + krow < 0) ktok = b * SEQ;
;               const bf16* kp = PROJ + (size_t)ktok * INW + C_KS + 64 * hk + 8 * g4; kf[j][0] = *(const GAS bf16x8*)kp; kf[j][1] = *(const GAS bf16x8*)(kp + 32); }
; #pragma unroll
;           for (int g = 0; g < 3; ++g) { const bf16* qp = PROJ + (size_t)(q0_ + c16) * INW + C_QS + 64 * (3 * hk + g) + 8 * g4; qf[g][0] = *(const GAS bf16x8*)qp; qf[g][1] = *(const GAS bf16x8*)(qp + 32); } }
.LBB0_531:
	s_or_b64 exec, exec, s[26:27]
	s_waitcnt vmcnt(0)
	v_lshlrev_b32_e32 v0, 16, v4
	s_mov_b32 s22, 0xffff
	v_lshrrev_b32_e32 v1, 16, v8
	s_mov_b32 s23, 0xffff0000
	v_and_or_b32 v0, v8, s22, v0
	v_and_or_b32 v1, v4, s23, v1
	ds_write2_b32 v220, v0, v1 offset1:132
	v_lshlrev_b32_e32 v0, 16, v5
	v_lshrrev_b32_e32 v1, 16, v9
	v_and_or_b32 v0, v9, s22, v0
	v_and_or_b32 v1, v5, s23, v1
	v_add_u32_e32 v3, 0x400, v220
	ds_write2_b32 v3, v0, v1 offset0:8 offset1:140
	v_lshlrev_b32_e32 v0, 16, v6
	v_lshrrev_b32_e32 v1, 16, v10
	v_and_or_b32 v0, v10, s22, v0
	v_and_or_b32 v1, v6, s23, v1
	v_add_u32_e32 v3, 0x800, v220
	ds_write2_b32 v3, v0, v1 offset0:16 offset1:148
	v_lshlrev_b32_e32 v0, 16, v7
	v_lshrrev_b32_e32 v1, 16, v11
	v_and_or_b32 v0, v11, s22, v0
	v_and_or_b32 v1, v7, s23, v1
	v_add_u32_e32 v3, 0xc00, v220
	v_readlane_b32 s22, v255, 16
	ds_write2_b32 v3, v0, v1 offset0:24 offset1:156
	v_add_u32_e32 v0, s35, v184
	v_mov_b32_e32 v3, s21
	v_readlane_b32 s23, v255, 17
	s_lshl_b32 s30, s20, 1
	v_readlane_b32 s20, v255, 18
	v_cndmask_b32_e64 v4, v0, v3, s[22:23]
	v_readlane_b32 s22, v254, 39
	v_readlane_b32 s23, v254, 40
	v_add_u32_e32 v12, s35, v187
	v_readlane_b32 s21, v255, 19
	v_mov_b64_e32 v[0:1], s[22:23]
	s_movk_i32 s26, 0x2400
	v_cndmask_b32_e64 v12, v12, v3, s[20:21]
	v_mad_i64_i32 v[12:13], s[20:21], v12, s26, v[0:1]
	v_readlane_b32 s20, v255, 20
	v_add_u32_e32 v20, s35, v188
	v_readlane_b32 s21, v255, 21
	v_add_u32_e32 v28, s35, v189
	v_add_u32_e32 v36, s35, v190
	v_cndmask_b32_e64 v20, v20, v3, s[20:21]
	v_mad_i64_i32 v[20:21], s[20:21], v20, s26, v[0:1]
	v_readlane_b32 s20, v255, 22
	v_readlane_b32 s21, v255, 23
	v_add_u32_e32 v44, s35, v191
	v_add_u32_e32 v52, s35, v192
	v_add_u32_e32 v56, s35, v193
	v_cndmask_b32_e64 v28, v28, v3, s[20:21]
	v_cndmask_b32_e64 v36, v36, v3, s[24:25]
	v_cndmask_b32_e64 v44, v44, v3, s[0:1]
	v_cndmask_b32_e64 v52, v52, v3, s[28:29]
	v_cndmask_b32_e64 v3, v56, v3, s[16:17]
	v_mad_i64_i32 v[56:57], s[20:21], v3, s26, v[0:1]
	v_add_u32_e32 v3, s35, v183
	v_mad_i64_i32 v[4:5], s[22:23], v4, s26, v[0:1]
	v_mad_i64_i32 v[28:29], s[20:21], v28, s26, v[0:1]
	v_mad_i64_i32 v[36:37], s[20:21], v36, s26, v[0:1]
	v_mad_i64_i32 v[44:45], s[20:21], v44, s26, v[0:1]
	v_mad_i64_i32 v[52:53], s[20:21], v52, s26, v[0:1]
	v_mad_i64_i32 v[0:1], s[20:21], v3, s26, v[0:1]
	v_lshl_add_u64 v[4:5], v[4:5], 0, s[30:31]
	v_lshl_add_u64 v[12:13], v[12:13], 0, s[30:31]
	v_lshl_add_u64 v[20:21], v[20:21], 0, s[30:31]
	v_lshl_add_u64 v[28:29], v[28:29], 0, s[30:31]
	v_lshl_add_u64 v[36:37], v[36:37], 0, s[30:31]
	v_lshl_add_u64 v[44:45], v[44:45], 0, s[30:31]
	v_lshl_add_u64 v[52:53], v[52:53], 0, s[30:31]
	v_lshl_add_u64 v[56:57], v[56:57], 0, s[30:31]
	v_lshl_add_u64 v[0:1], v[0:1], 0, s[30:31]
	v_lshl_add_u64 v[8:9], v[4:5], 0, v[178:179]
	v_lshl_add_u64 v[16:17], v[12:13], 0, v[178:179]
	v_lshl_add_u64 v[24:25], v[20:21], 0, v[178:179]
	v_lshl_add_u64 v[32:33], v[28:29], 0, v[178:179]
	v_lshl_add_u64 v[40:41], v[36:37], 0, v[178:179]
	v_lshl_add_u64 v[48:49], v[44:45], 0, v[178:179]
	v_lshl_add_u64 v[52:53], v[52:53], 0, v[178:179]
	v_lshl_add_u64 v[56:57], v[56:57], 0, v[178:179]
	v_lshl_add_u64 v[0:1], v[0:1], 0, v[178:179]
	v_add_u32_e32 v3, s35, v182
	global_load_dwordx4 v[4:7], v[8:9], off offset:3584
	s_nop 0
	global_load_dwordx4 v[8:11], v[8:9], off offset:3648
	s_nop 0
	global_load_dwordx4 v[12:15], v[16:17], off offset:3584
	s_nop 0
	global_load_dwordx4 v[16:19], v[16:17], off offset:3648
	s_nop 0
	global_load_dwordx4 v[20:23], v[24:25], off offset:3584
	s_nop 0
	global_load_dwordx4 v[24:27], v[24:25], off offset:3648
	s_nop 0
	global_load_dwordx4 v[28:31], v[32:33], off offset:3584
	s_nop 0
	global_load_dwordx4 v[32:35], v[32:33], off offset:3648
	s_nop 0
	global_load_dwordx4 v[36:39], v[40:41], off offset:3584
	s_nop 0
	global_load_dwordx4 v[40:43], v[40:41], off offset:3648
	s_nop 0
	global_load_dwordx4 v[44:47], v[48:49], off offset:3584
	s_nop 0
	global_load_dwordx4 v[48:51], v[48:49], off offset:3648
	s_nop 0
	global_load_dwordx4 v[60:63], v[52:53], off offset:3584
	s_nop 0
	global_load_dwordx4 v[52:55], v[52:53], off offset:3648
	s_nop 0
	global_load_dwordx4 v[64:67], v[56:57], off offset:3584
	s_nop 0
	global_load_dwordx4 v[56:59], v[56:57], off offset:3648
	s_nop 0
	global_load_dwordx4 v[72:75], v[0:1], off offset:3584
	global_load_dwordx4 v[68:71], v[0:1], off offset:3648
	v_mad_i64_i32 v[0:1], s[22:23], v3, s26, v[176:177]
	s_mul_i32 s30, s34, 0x180
	v_lshl_add_u64 v[76:77], v[0:1], 0, s[30:31]
	global_load_dwordx4 v[88:91], v[76:77], off offset:2048
	global_load_dwordx4 v[84:87], v[76:77], off offset:2112
	s_mul_i32 s20, s34, 3
	s_lshl_b32 s21, s20, 7
	s_add_i32 s26, s21, 0x80
	s_mov_b32 s27, s31
	s_add_i32 s34, s21, 0x100
	s_mov_b32 s35, s31
	s_lshl_b32 s20, s20, 2
	v_lshl_add_u64 v[76:77], v[0:1], 0, s[26:27]
	v_lshl_add_u64 v[0:1], v[0:1], 0, s[34:35]
	s_movk_i32 s21, 0x600
	v_mov_b32_e32 v221, s20
	global_load_dwordx4 v[168:171], v[76:77], off offset:2048
	global_load_dwordx4 v[164:167], v[76:77], off offset:2112
	global_load_dwordx4 v[80:83], v[0:1], off offset:2048
	s_nop 0
	global_load_dwordx4 v[76:79], v[0:1], off offset:2112
	s_waitcnt lgkmcnt(0)
	s_barrier
; #define MFMA16(a, b, c) __builtin_amdgcn_mfma_f32_16x16x32_bf16(a, b, c, 0, 0, 0)
; __device__ __forceinline__ void swa_phase(const Ctx& C, const bf16* PROJ, const float* sinks, bf16* YSWA) {
;     ...
;         for (int g = 0; g < 3; ++g) {
;             const int h = 3 * hk + g; const float sink2 = sinks[h] * LOG2E;
;             const int q0 = tb + 16 * w;
;             f32x4 s[9];
; #pragma unroll
;             for (int j = 0; j < 9; ++j) { f32x4 a = {0.f, 0.f, 0.f, 0.f}; a = MFMA16(kf[j][0], qf[g][0], a); a = MFMA16(kf[j][1], qf[g][1], a); s[j] = a; }
;             const int qr = 16 * w + c16; float mx = -INFINITY;
; #pragma unroll
;             for (int j = 0; j < 9; ++j)
; #pragma unroll
;                 for (int r = 0; r < 4; ++r) { const int kr = 16 * w - 128 + 16 * j + 4 * g4 + r, diff = qr - kr; const bool ok = diff >= 0 && diff < 128 && (128 * n + kr) >= 0;
;                     s[j][r] = ok ? s[j][r] : -INFINITY; mx = fmaxf(mx, s[j][r]); }
;             mx = fmaxf(mx, __shfl_xor(mx, 16)); mx = fmaxf(mx, __shfl_xor(mx, 32)); mx = fmaxf(mx, sink2);
;             float sum = 0.f;
; #pragma unroll
;             for (int j = 0; j < 9; ++j)
; #pragma unroll
;                 for (int r = 0; r < 4; ++r) { const float e = __builtin_amdgcn_exp2f(s[j][r] - mx); s[j][r] = e; sum += e; }
;             sum += __shfl_xor(sum, 16); sum += __shfl_xor(sum, 32); sum += __builtin_amdgcn_exp2f(sink2 - mx);
	v_mad_i64_i32 v[180:181], s[22:23], v3, s21, v[172:173]
	global_load_dword v3, v221, s[36:37]
	s_waitcnt vmcnt(6)
	v_mfma_f32_16x16x32_bf16 v[92:95], v[4:7], v[88:91], 0
	s_mov_b32 s22, 0xff800000
	s_mov_b32 s23, 0x3fb8aa3b
	s_addk_i32 s18, 0x2000
	v_mfma_f32_16x16x32_bf16 v[96:99], v[12:15], v[88:91], 0
	s_waitcnt vmcnt(5)
	v_mfma_f32_16x16x32_bf16 v[92:95], v[8:11], v[84:87], v[92:95]
	v_mfma_f32_16x16x32_bf16 v[100:103], v[20:23], v[88:91], 0
	v_mfma_f32_16x16x32_bf16 v[104:107], v[28:31], v[88:91], 0
	s_nop 5
	v_cndmask_b32_e64 v0, v216, v92, s[40:41]
	v_cndmask_b32_e64 v1, v216, v93, s[42:43]
	v_mfma_f32_16x16x32_bf16 v[108:111], v[36:39], v[88:91], 0
	v_mfma_f32_16x16x32_bf16 v[112:115], v[44:47], v[88:91], 0
	v_mfma_f32_16x16x32_bf16 v[116:119], v[60:63], v[88:91], 0
	v_mfma_f32_16x16x32_bf16 v[120:123], v[64:67], v[88:91], 0
	v_mfma_f32_16x16x32_bf16 v[88:91], v[72:75], v[88:91], 0
	v_mfma_f32_16x16x32_bf16 v[96:99], v[16:19], v[84:87], v[96:99]
	v_mfma_f32_16x16x32_bf16 v[100:103], v[24:27], v[84:87], v[100:103]
	v_mfma_f32_16x16x32_bf16 v[104:107], v[32:35], v[84:87], v[104:107]
	s_nop 5
	v_cndmask_b32_e64 v92, v216, v97, s[50:51]
	v_cndmask_b32_e64 v93, v216, v98, s[52:53]
	v_cndmask_b32_e64 v97, v216, v102, s[60:61]
	v_mfma_f32_16x16x32_bf16 v[108:111], v[40:43], v[84:87], v[108:111]
	v_cndmask_b32_e64 v98, v216, v103, s[62:63]
	v_cndmask_b32_e64 v102, v216, v107, s[70:71]
	v_mfma_f32_16x16x32_bf16 v[112:115], v[48:51], v[84:87], v[112:115]
	v_mfma_f32_16x16x32_bf16 v[116:119], v[52:55], v[84:87], v[116:119]
	s_nop 3
	v_cndmask_b32_e64 v103, v216, v108, s[72:73]
	s_nop 1
	v_cndmask_b32_e64 v107, v216, v112, s[80:81]
	v_cndmask_b32_e64 v108, v216, v113, s[82:83]
	v_mfma_f32_16x16x32_bf16 v[120:123], v[56:59], v[84:87], v[120:123]
	v_mfma_f32_16x16x32_bf16 v[84:87], v[68:71], v[84:87], v[88:91]
	v_cndmask_b32_e64 v112, v216, v117, s[90:91]
	v_cndmask_b32_e64 v113, v216, v118, s[92:93]
	s_nop 4
	v_cndmask_b32_e64 v117, v216, v122, s[4:5]
	v_max3_f32 v88, v0, s22, v1
	v_cndmask_b32_e64 v89, v216, v94, s[44:45]
	v_cndmask_b32_e64 v90, v216, v95, s[46:47]
	v_max3_f32 v88, v88, v89, v90
	v_cndmask_b32_e64 v91, v216, v96, s[48:49]
	v_max3_f32 v88, v88, v91, v92
	v_cndmask_b32_e64 v94, v216, v99, s[54:55]
	v_max3_f32 v88, v88, v93, v94
	v_cndmask_b32_e64 v95, v216, v100, s[56:57]
	v_cndmask_b32_e64 v96, v216, v101, s[58:59]
	v_max3_f32 v88, v88, v95, v96
	v_max3_f32 v88, v88, v97, v98
	v_cndmask_b32_e64 v99, v216, v104, s[64:65]
	v_cndmask_b32_e64 v100, v216, v105, s[66:67]
	v_max3_f32 v88, v88, v99, v100
	v_cndmask_b32_e64 v101, v216, v106, s[68:69]
	v_max3_f32 v88, v88, v101, v102
	v_cndmask_b32_e64 v104, v216, v109, s[74:75]
	v_max3_f32 v88, v88, v103, v104
	v_cndmask_b32_e64 v105, v216, v110, s[76:77]
	v_cndmask_b32_e64 v106, v216, v111, s[78:79]
	v_max3_f32 v88, v88, v105, v106
	v_max3_f32 v88, v88, v107, v108
	v_cndmask_b32_e64 v109, v216, v114, s[84:85]
	v_cndmask_b32_e64 v110, v216, v115, s[86:87]
	v_max3_f32 v88, v88, v109, v110
	v_cndmask_b32_e64 v111, v216, v116, s[88:89]
	v_max3_f32 v88, v88, v111, v112
	v_cndmask_b32_e64 v114, v216, v119, s[94:95]
	v_max3_f32 v88, v88, v113, v114
	v_cndmask_b32_e64 v115, v216, v120, s[96:97]
	v_cndmask_b32_e64 v116, v216, v121, s[2:3]
	v_max3_f32 v88, v88, v115, v116
	v_cndmask_b32_e64 v118, v216, v123, s[6:7]
	v_max3_f32 v88, v88, v117, v118
	v_cndmask_b32_e64 v119, v216, v84, s[8:9]
	v_cndmask_b32_e64 v120, v216, v85, s[10:11]
	v_max3_f32 v84, v88, v119, v120
	v_cndmask_b32_e64 v121, v216, v86, s[12:13]
	v_cndmask_b32_e64 v122, v216, v87, s[14:15]
	v_max3_f32 v84, v84, v121, v122
	v_mov_b32_e32 v86, v84
	s_nop 1
	v_permlane16_swap_b32_e32 v86, v84
	s_waitcnt vmcnt(0)
	v_mul_f32_e32 v85, 0x3fb8aa3b, v3
	v_mfma_f32_16x16x32_bf16 v[242:245], v[44:47], v[168:171], 0
	s_waitcnt lgkmcnt(0)
	v_max_f32_e32 v84, v84, v86
	v_mov_b32_e32 v86, v84
	s_nop 1
	v_permlane32_swap_b32_e32 v86, v84
	v_mfma_f32_16x16x32_bf16 v[246:249], v[60:63], v[168:171], 0
	s_waitcnt lgkmcnt(0)
	v_max3_f32 v123, v84, v86, v85
	v_sub_f32_e32 v88, v93, v123
	v_sub_f32_e32 v93, v98, v123
	v_sub_f32_e32 v98, v103, v123
	v_sub_f32_e32 v103, v108, v123
	v_sub_f32_e32 v108, v113, v123
	v_sub_f32_e32 v87, v92, v123
	v_sub_f32_e32 v92, v97, v123
	v_sub_f32_e32 v97, v102, v123
	v_sub_f32_e32 v102, v107, v123
	v_sub_f32_e32 v107, v112, v123
	v_exp_f32_e32 v112, v108
	v_sub_f32_e32 v108, v114, v123
	v_exp_f32_e32 v113, v108
	v_sub_f32_e32 v108, v115, v123
	v_exp_f32_e32 v114, v108
	v_sub_f32_e32 v108, v116, v123
	v_exp_f32_e32 v115, v108
	v_sub_f32_e32 v108, v117, v123
	v_sub_f32_e32 v0, v0, v123
	v_exp_f32_e32 v116, v108
	v_sub_f32_e32 v108, v118, v123
	v_exp_f32_e32 v0, v0
	v_sub_f32_e32 v1, v1, v123
	v_exp_f32_e32 v117, v108
	v_sub_f32_e32 v108, v119, v123
	v_exp_f32_e32 v1, v1
	v_sub_f32_e32 v84, v89, v123
	v_exp_f32_e32 v118, v108
	v_sub_f32_e32 v108, v120, v123
	v_exp_f32_e32 v84, v84
	v_sub_f32_e32 v85, v90, v123
	v_exp_f32_e32 v119, v108
	v_sub_f32_e32 v108, v121, v123
	v_exp_f32_e32 v85, v85
	v_sub_f32_e32 v86, v91, v123
	v_exp_f32_e32 v120, v108
	v_sub_f32_e32 v108, v122, v123
	v_exp_f32_e32 v86, v86
	v_exp_f32_e32 v121, v108
	v_add_f32_e32 v108, 0, v0
	v_exp_f32_e32 v87, v87
	v_add_f32_e32 v108, v1, v108
	v_exp_f32_e32 v88, v88
	v_sub_f32_e32 v89, v94, v123
	v_add_f32_e32 v108, v84, v108
	v_exp_f32_e32 v89, v89
	v_sub_f32_e32 v90, v95, v123
	v_add_f32_e32 v108, v85, v108
	v_exp_f32_e32 v90, v90
	v_sub_f32_e32 v91, v96, v123
	v_add_f32_e32 v108, v86, v108
	v_exp_f32_e32 v91, v91
	v_add_f32_e32 v108, v87, v108
	v_exp_f32_e32 v92, v92
	v_add_f32_e32 v108, v88, v108
	v_exp_f32_e32 v93, v93
	v_sub_f32_e32 v94, v99, v123
; #define LAS __attribute__((address_space(3)))
; __device__ __forceinline__ unsigned pk2(float lo, float hi) { f32x2_m v = {lo, hi}; bf16x2_m b = __builtin_convertvector(v, bf16x2_m); return __builtin_bit_cast(unsigned, b); }
; #define MFMA16(a, b, c) __builtin_amdgcn_mfma_f32_16x16x32_bf16(a, b, c, 0, 0, 0)
; __device__ __forceinline__ void swa_phase(const Ctx& C, const bf16* PROJ, const float* sinks, bf16* YSWA) {
;     ...
;                 for (int r = 0; r < 4; ++r) { const float e = __builtin_amdgcn_exp2f(s[j][r] - mx); s[j][r] = e; sum += e; }
;             sum += __shfl_xor(sum, 16); sum += __shfl_xor(sum, 32); sum += __builtin_amdgcn_exp2f(sink2 - mx);
;             const float inv = 1.0f / sum;
;             unsigned pw[10][2];
; #pragma unroll
;             for (int j = 0; j < 9; ++j) { pw[j][0] = pk2(s[j][0] * inv, s[j][1] * inv); pw[j][1] = pk2(s[j][2] * inv, s[j][3] * inv); }
;             pw[9][0] = 0u; pw[9][1] = 0u;
;             f32x4 o[4];
; #pragma unroll
;             for (int dt = 0; dt < 4; ++dt) o[dt] = (f32x4){0.f, 0.f, 0.f, 0.f};
; #pragma unroll
;             for (int sI = 0; sI < 5; ++sI) {
;                 const v4u pb = {pw[2 * sI][0], pw[2 * sI][1], pw[2 * sI + 1][0], pw[2 * sI + 1][1]};
;                 const int kkA = 16 * w + 32 * sI + 4 * g4; int kkB = kkA + 16; if (kkB > 252) kkB = 252;
; #pragma unroll
;                 for (int dt = 0; dt < 4; ++dt) { const LAS bf16* vp = vt + (16 * dt + c16) * 264;
;                     const v2u va = *(const LAS v2u*)(vp + kkA), vb = *(const LAS v2u*)(vp + kkB);
;                     const v4u av = {va.x, va.y, vb.x, vb.y};
;                     o[dt] = MFMA16(__builtin_bit_cast(bf16x8, av), __builtin_bit_cast(bf16x8, pb), o[dt]); }
	v_add_f32_e32 v108, v89, v108
	v_exp_f32_e32 v94, v94
	v_sub_f32_e32 v95, v100, v123
	v_add_f32_e32 v108, v90, v108
	v_exp_f32_e32 v95, v95
	v_sub_f32_e32 v96, v101, v123
	v_add_f32_e32 v108, v91, v108
	v_exp_f32_e32 v96, v96
	v_add_f32_e32 v108, v92, v108
	v_exp_f32_e32 v97, v97
	v_add_f32_e32 v108, v93, v108
	v_exp_f32_e32 v98, v98
	v_sub_f32_e32 v99, v104, v123
	v_add_f32_e32 v108, v94, v108
	v_exp_f32_e32 v99, v99
	v_sub_f32_e32 v100, v105, v123
	v_add_f32_e32 v108, v95, v108
	v_exp_f32_e32 v100, v100
	v_sub_f32_e32 v101, v106, v123
	v_add_f32_e32 v108, v96, v108
	v_exp_f32_e32 v101, v101
	v_add_f32_e32 v108, v97, v108
	v_exp_f32_e32 v102, v102
	v_add_f32_e32 v108, v98, v108
	v_exp_f32_e32 v103, v103
	v_sub_f32_e32 v104, v109, v123
	v_add_f32_e32 v108, v99, v108
	v_exp_f32_e32 v104, v104
	v_sub_f32_e32 v105, v110, v123
	v_add_f32_e32 v108, v100, v108
	v_exp_f32_e32 v105, v105
	v_sub_f32_e32 v106, v111, v123
	v_add_f32_e32 v108, v101, v108
	v_exp_f32_e32 v106, v106
	v_add_f32_e32 v108, v102, v108
	v_exp_f32_e32 v107, v107
	v_add_f32_e32 v108, v103, v108
	v_add_f32_e32 v108, v104, v108
	v_add_f32_e32 v108, v105, v108
	v_add_f32_e32 v108, v106, v108
	v_add_f32_e32 v108, v107, v108
	v_add_f32_e32 v108, v112, v108
	v_add_f32_e32 v108, v113, v108
	v_add_f32_e32 v108, v114, v108
	v_add_f32_e32 v108, v115, v108
	v_add_f32_e32 v108, v116, v108
	v_add_f32_e32 v108, v117, v108
	v_add_f32_e32 v108, v118, v108
	v_add_f32_e32 v108, v119, v108
	v_add_f32_e32 v108, v120, v108
	v_add_f32_e32 v108, v121, v108
	v_mov_b32_e32 v109, v108
	s_nop 1
	v_permlane16_swap_b32_e32 v109, v108
	v_fma_f32 v3, v3, s23, -v123
	v_exp_f32_e32 v3, v3
	v_mfma_f32_16x16x32_bf16 v[242:245], v[48:51], v[164:167], v[242:245]
	s_waitcnt lgkmcnt(0)
	v_add_f32_e32 v108, v108, v109
	v_mov_b32_e32 v109, v108
	s_nop 1
	v_permlane32_swap_b32_e32 v109, v108
	v_mfma_f32_16x16x32_bf16 v[246:249], v[52:55], v[164:167], v[246:249]
	s_waitcnt lgkmcnt(0)
	v_add_f32_e32 v108, v108, v109
	v_add_f32_e32 v3, v3, v108
	v_div_scale_f32 v108, s[20:21], v3, v3, 1.0
	v_rcp_f32_e32 v109, v108
	s_nop 0
	v_fma_f32 v110, -v108, v109, 1.0
	v_fmac_f32_e32 v109, v110, v109
	v_div_scale_f32 v110, vcc, 1.0, v3, 1.0
	v_mul_f32_e32 v111, v110, v109
	v_fma_f32 v122, -v108, v111, v110
	v_fmac_f32_e32 v111, v122, v109
	v_fma_f32 v108, -v108, v111, v110
	v_div_fmas_f32 v108, v108, v109, v111
	v_div_fixup_f32 v122, v108, v3, 1.0
	v_pk_mul_f32 v[0:1], v[0:1], v[122:123] op_sel_hi:[1,0]
	v_add_u32_e32 v3, 0x100, v194
	v_cvt_pk_bf16_f32 v108, v0, v1
	v_pk_mul_f32 v[0:1], v[84:85], v[122:123] op_sel_hi:[1,0]
	v_pk_mul_f32 v[84:85], v[120:121], v[122:123] op_sel_hi:[1,0]
	v_cvt_pk_bf16_f32 v109, v0, v1
	v_pk_mul_f32 v[0:1], v[86:87], v[122:123] op_sel_hi:[1,0]
	s_nop 0
	v_cvt_pk_bf16_f32 v110, v0, v1
	v_pk_mul_f32 v[0:1], v[88:89], v[122:123] op_sel_hi:[1,0]
	s_nop 0
	v_cvt_pk_bf16_f32 v111, v0, v1
	v_pk_mul_f32 v[0:1], v[90:91], v[122:123] op_sel_hi:[1,0]
	s_nop 0
	v_cvt_pk_bf16_f32 v124, v0, v1
	v_pk_mul_f32 v[0:1], v[92:93], v[122:123] op_sel_hi:[1,0]
	s_nop 0
	v_cvt_pk_bf16_f32 v125, v0, v1
	v_pk_mul_f32 v[0:1], v[94:95], v[122:123] op_sel_hi:[1,0]
	s_nop 0
	v_cvt_pk_bf16_f32 v126, v0, v1
	v_pk_mul_f32 v[0:1], v[96:97], v[122:123] op_sel_hi:[1,0]
	s_nop 0
	v_cvt_pk_bf16_f32 v127, v0, v1
	v_pk_mul_f32 v[0:1], v[98:99], v[122:123] op_sel_hi:[1,0]
	s_nop 0
	v_cvt_pk_bf16_f32 v140, v0, v1
	v_pk_mul_f32 v[0:1], v[100:101], v[122:123] op_sel_hi:[1,0]
	s_nop 0
	v_cvt_pk_bf16_f32 v141, v0, v1
	v_pk_mul_f32 v[0:1], v[102:103], v[122:123] op_sel_hi:[1,0]
	s_nop 0
	v_cvt_pk_bf16_f32 v142, v0, v1
	v_pk_mul_f32 v[0:1], v[104:105], v[122:123] op_sel_hi:[1,0]
	s_nop 0
	v_cvt_pk_bf16_f32 v143, v0, v1
	v_pk_mul_f32 v[0:1], v[106:107], v[122:123] op_sel_hi:[1,0]
	s_nop 0
	v_cvt_pk_bf16_f32 v156, v0, v1
	v_pk_mul_f32 v[0:1], v[112:113], v[122:123] op_sel_hi:[1,0]
	s_nop 0
	v_cvt_pk_bf16_f32 v157, v0, v1
	v_pk_mul_f32 v[0:1], v[114:115], v[122:123] op_sel_hi:[1,0]
	ds_read2_b64 v[112:115], v194 offset1:8
	ds_read_b64 v[94:95], v195 offset:32
	v_cvt_pk_bf16_f32 v158, v0, v1
	v_pk_mul_f32 v[0:1], v[116:117], v[122:123] op_sel_hi:[1,0]
	s_waitcnt lgkmcnt(1)
	v_mov_b32_e32 v92, v112
	v_cvt_pk_bf16_f32 v159, v0, v1
	v_pk_mul_f32 v[0:1], v[118:119], v[122:123] op_sel_hi:[1,0]
	v_mov_b32_e32 v93, v113
	v_cvt_pk_bf16_f32 v0, v0, v1
	v_cvt_pk_bf16_f32 v1, v84, v85
	ds_read2st64_b64 v[84:87], v3 offset1:16
	ds_read_b64 v[98:99], v195 offset:8480
	s_waitcnt lgkmcnt(2)
	v_mfma_f32_16x16x32_bf16 v[116:119], v[92:95], v[108:111], 0
	s_waitcnt lgkmcnt(1)
	v_mov_b32_e32 v96, v86
	v_add_u32_e32 v86, 0x4000, v194
	ds_read2_b64 v[128:131], v86 offset0:64 offset1:72
	ds_read_b64 v[102:103], v195 offset:16928
	ds_read2st64_b64 v[88:91], v3 offset0:33 offset1:49
	ds_read_b64 v[106:107], v195 offset:25376
	v_mov_b32_e32 v97, v87
	v_add_u32_e32 v3, 0x2000, v194
	s_waitcnt lgkmcnt(3)
	v_mov_b32_e32 v100, v128
	v_mov_b32_e32 v101, v129
	s_waitcnt lgkmcnt(1)
	v_mov_b32_e32 v104, v90
	v_mov_b32_e32 v105, v91
	v_mfma_f32_16x16x32_bf16 v[120:123], v[96:99], v[108:111], 0
	v_add_u32_e32 v87, 0x6000, v194
	v_mfma_f32_16x16x32_bf16 v[132:135], v[100:103], v[108:111], 0
	s_waitcnt lgkmcnt(0)
	v_mfma_f32_16x16x32_bf16 v[136:139], v[104:107], v[108:111], 0
	ds_read_b64 v[110:111], v196 offset:32
	v_mov_b32_e32 v108, v114
	v_mov_b32_e32 v109, v115
	ds_read2_b64 v[148:151], v3 offset0:40 offset1:48
	ds_read_b64 v[114:115], v196 offset:8480
	s_waitcnt lgkmcnt(2)
	v_mfma_f32_16x16x32_bf16 v[144:147], v[108:111], v[124:127], v[116:119]
	s_waitcnt lgkmcnt(1)
	v_mov_b32_e32 v112, v148
	v_mov_b32_e32 v113, v149
	ds_read_b64 v[118:119], v196 offset:16928
	v_mov_b32_e32 v116, v130
	s_waitcnt lgkmcnt(1)
; #define GAS __attribute__((address_space(1)))
; #define LAS __attribute__((address_space(3)))
; __device__ __forceinline__ unsigned pk2(float lo, float hi) { f32x2_m v = {lo, hi}; bf16x2_m b = __builtin_convertvector(v, bf16x2_m); return __builtin_bit_cast(unsigned, b); }
; #define MFMA16(a, b, c) __builtin_amdgcn_mfma_f32_16x16x32_bf16(a, b, c, 0, 0, 0)
; __device__ __forceinline__ void swa_phase(const Ctx& C, const bf16* PROJ, const float* sinks, bf16* YSWA) {
;     ...
;             const int h = 3 * hk + g; const float sink2 = sinks[h] * LOG2E;
;             const int q0 = tb + 16 * w;
;             f32x4 s[9];
; #pragma unroll
;             for (int j = 0; j < 9; ++j) { f32x4 a = {0.f, 0.f, 0.f, 0.f}; a = MFMA16(kf[j][0], qf[g][0], a); a = MFMA16(kf[j][1], qf[g][1], a); s[j] = a; }
;             const int qr = 16 * w + c16; float mx = -INFINITY;
; #pragma unroll
;             for (int j = 0; j < 9; ++j)
; #pragma unroll
;                 for (int r = 0; r < 4; ++r) { const int kr = 16 * w - 128 + 16 * j + 4 * g4 + r, diff = qr - kr; const bool ok = diff >= 0 && diff < 128 && (128 * n + kr) >= 0;
;                     s[j][r] = ok ? s[j][r] : -INFINITY; mx = fmaxf(mx, s[j][r]); }
;             mx = fmaxf(mx, __shfl_xor(mx, 16)); mx = fmaxf(mx, __shfl_xor(mx, 32)); mx = fmaxf(mx, sink2);
;     ...
;                 const v4u pb = {pw[2 * sI][0], pw[2 * sI][1], pw[2 * sI + 1][0], pw[2 * sI + 1][1]};
;                 const int kkA = 16 * w + 32 * sI + 4 * g4; int kkB = kkA + 16; if (kkB > 252) kkB = 252;
; #pragma unroll
;                 for (int dt = 0; dt < 4; ++dt) { const LAS bf16* vp = vt + (16 * dt + c16) * 264;
;                     const v2u va = *(const LAS v2u*)(vp + kkA), vb = *(const LAS v2u*)(vp + kkB);
;                     const v4u av = {va.x, va.y, vb.x, vb.y};
;                     o[dt] = MFMA16(__builtin_bit_cast(bf16x8, av), __builtin_bit_cast(bf16x8, pb), o[dt]); }
;             }
;             bf16* op = YSWA + (size_t)(q0 + c16) * 768 + 64 * h + 4 * g4;
; #pragma unroll
;             for (int dt = 0; dt < 4; ++dt) { v2u wv; wv.x = pk2(o[dt][0], o[dt][1]); wv.y = pk2(o[dt][2], o[dt][3]); *(GAS v2u*)(op + 16 * dt) = wv; }
	v_mfma_f32_16x16x32_bf16 v[152:155], v[112:115], v[124:127], v[120:123]
	ds_read2_b64 v[222:225], v87 offset0:104 offset1:112
	s_nop 1
	ds_read_b64 v[122:123], v196 offset:25376
	v_mov_b32_e32 v117, v131
	v_mov_b32_e32 v128, v150
	v_mov_b32_e32 v129, v151
	s_waitcnt lgkmcnt(1)
	v_mov_b32_e32 v120, v222
	v_mov_b32_e32 v121, v223
	v_mfma_f32_16x16x32_bf16 v[160:163], v[116:119], v[124:127], v[132:135]
	s_waitcnt lgkmcnt(0)
	v_mfma_f32_16x16x32_bf16 v[226:229], v[120:123], v[124:127], v[136:139]
	ds_read2_b64 v[230:233], v194 offset0:16 offset1:24
	ds_read_b64 v[126:127], v197 offset:32
	ds_read_b64 v[130:131], v197 offset:8480
	v_mov_b32_e32 v136, v224
	s_waitcnt lgkmcnt(0)
	v_mfma_f32_16x16x32_bf16 v[148:151], v[128:131], v[140:143], v[152:155]
	s_nop 2
	ds_read2_b64 v[152:155], v86 offset0:80 offset1:88
	ds_read_b64 v[134:135], v197 offset:16928
	ds_read_b64 v[138:139], v197 offset:25376
	v_mov_b32_e32 v124, v230
	v_mov_b32_e32 v125, v231
	s_waitcnt lgkmcnt(2)
	v_mov_b32_e32 v132, v152
	v_mov_b32_e32 v133, v153
	v_mov_b32_e32 v137, v225
	v_mfma_f32_16x16x32_bf16 v[144:147], v[124:127], v[140:143], v[144:147]
	s_waitcnt lgkmcnt(1)
	v_mfma_f32_16x16x32_bf16 v[160:163], v[132:135], v[140:143], v[160:163]
	s_waitcnt lgkmcnt(0)
	v_mfma_f32_16x16x32_bf16 v[222:225], v[136:139], v[140:143], v[226:229]
	ds_read_b64 v[142:143], v204 offset:32
	v_mov_b32_e32 v140, v232
	v_mov_b32_e32 v141, v233
	s_waitcnt lgkmcnt(0)
	s_nop 0
	v_mfma_f32_16x16x32_bf16 v[226:229], v[140:143], v[156:159], v[144:147]
	ds_read2_b64 v[230:233], v3 offset0:56 offset1:64
	s_nop 1
	ds_read_b64 v[146:147], v204 offset:8480
	v_mov_b32_e32 v3, v2
	s_waitcnt lgkmcnt(1)
	v_mov_b32_e32 v144, v230
	v_mov_b32_e32 v145, v231
	s_waitcnt lgkmcnt(0)
	s_nop 0
	v_mfma_f32_16x16x32_bf16 v[234:237], v[144:147], v[156:159], v[148:151]
	s_nop 2
	ds_read_b64 v[150:151], v204 offset:16928
	v_mov_b32_e32 v148, v154
	v_mov_b32_e32 v149, v155
	ds_read2_b64 v[238:241], v87 offset0:120 offset1:128
	ds_read_b64 v[154:155], v204 offset:25376
	s_waitcnt lgkmcnt(2)
	v_mfma_f32_16x16x32_bf16 v[160:163], v[148:151], v[156:159], v[160:163]
	s_waitcnt lgkmcnt(1)
	v_mov_b32_e32 v152, v238
	v_mov_b32_e32 v153, v239
	ds_read_b64 v[86:87], v205 offset:32
	ds_read_b64 v[90:91], v205 offset:16928
	s_waitcnt lgkmcnt(2)
	v_mfma_f32_16x16x32_bf16 v[222:225], v[152:155], v[156:159], v[222:225]
	ds_read_b64 v[158:159], v205 offset:8480
	v_mov_b32_e32 v156, v232
	v_mov_b32_e32 v157, v233
	s_waitcnt lgkmcnt(2)
	v_mfma_f32_16x16x32_bf16 v[226:229], v[84:87], v[0:3], v[226:229]
	s_waitcnt lgkmcnt(0)
	v_mfma_f32_16x16x32_bf16 v[230:233], v[156:159], v[0:3], v[234:237]
	s_nop 5
	v_cvt_pk_bf16_f32 v198, v226, v227
	v_cvt_pk_bf16_f32 v199, v228, v229
	v_mfma_f32_16x16x32_bf16 v[234:237], v[88:91], v[0:3], v[160:163]
	s_nop 2
	ds_read_b64 v[162:163], v205 offset:25376
	v_mov_b32_e32 v160, v240
	v_mov_b32_e32 v161, v241
	v_mfma_f32_16x16x32_bf16 v[226:229], v[12:15], v[168:171], 0
	s_waitcnt lgkmcnt(0)
	v_mfma_f32_16x16x32_bf16 v[222:225], v[160:163], v[0:3], v[222:225]
	v_lshl_add_u64 v[0:1], v[180:181], 0, s[30:31]
	global_store_dwordx2 v[0:1], v[198:199], off
	v_cvt_pk_bf16_f32 v198, v230, v231
	v_cvt_pk_bf16_f32 v199, v232, v233
	global_store_dwordx2 v[0:1], v[198:199], off offset:32
	v_cvt_pk_bf16_f32 v198, v234, v235
	v_cvt_pk_bf16_f32 v199, v236, v237
	global_store_dwordx2 v[0:1], v[198:199], off offset:64
	v_cvt_pk_bf16_f32 v198, v222, v223
	v_cvt_pk_bf16_f32 v199, v224, v225
	global_store_dwordx2 v[0:1], v[198:199], off offset:96
	global_load_dword v3, v221, s[36:37] offset:4
	v_mfma_f32_16x16x32_bf16 v[222:225], v[4:7], v[168:171], 0
	v_mfma_f32_16x16x32_bf16 v[222:225], v[8:11], v[164:167], v[222:225]
	v_mfma_f32_16x16x32_bf16 v[230:233], v[20:23], v[168:171], 0
	v_mfma_f32_16x16x32_bf16 v[234:237], v[28:31], v[168:171], 0
	s_nop 5
	v_cndmask_b32_e64 v0, v216, v222, s[40:41]
	v_cndmask_b32_e64 v1, v216, v223, s[42:43]
	v_mfma_f32_16x16x32_bf16 v[238:241], v[36:39], v[168:171], 0
	v_mfma_f32_16x16x32_bf16 v[198:201], v[64:67], v[168:171], 0
	v_mfma_f32_16x16x32_bf16 v[168:171], v[72:75], v[168:171], 0
	v_mfma_f32_16x16x32_bf16 v[226:229], v[16:19], v[164:167], v[226:229]
	v_mfma_f32_16x16x32_bf16 v[230:233], v[24:27], v[164:167], v[230:233]
	v_mfma_f32_16x16x32_bf16 v[234:237], v[32:35], v[164:167], v[234:237]
	s_nop 5
	v_cndmask_b32_e64 v222, v216, v227, s[50:51]
	v_cndmask_b32_e64 v223, v216, v228, s[52:53]
	v_cndmask_b32_e64 v227, v216, v232, s[60:61]
	v_mfma_f32_16x16x32_bf16 v[238:241], v[40:43], v[164:167], v[238:241]
	v_cndmask_b32_e64 v228, v216, v233, s[62:63]
	v_cndmask_b32_e64 v232, v216, v237, s[70:71]
	v_cndmask_b32_e64 v237, v216, v242, s[80:81]
	v_mfma_f32_16x16x32_bf16 v[198:201], v[56:59], v[164:167], v[198:201]
	v_cndmask_b32_e64 v242, v216, v247, s[90:91]
	s_nop 2
	v_cndmask_b32_e64 v233, v216, v238, s[72:73]
	v_cndmask_b32_e64 v238, v216, v243, s[82:83]
	v_mfma_f32_16x16x32_bf16 v[164:167], v[68:71], v[164:167], v[168:171]
	v_cndmask_b32_e64 v243, v216, v248, s[92:93]
	v_cndmask_b32_e64 v247, v216, v200, s[4:5]
	v_cndmask_b32_e64 v248, v216, v201, s[6:7]
	v_max3_f32 v168, v0, s22, v1
	v_cndmask_b32_e64 v169, v216, v224, s[44:45]
	v_cndmask_b32_e64 v170, v216, v225, s[46:47]
	v_max3_f32 v168, v168, v169, v170
	v_cndmask_b32_e64 v171, v216, v226, s[48:49]
	v_max3_f32 v168, v168, v171, v222
	v_cndmask_b32_e64 v224, v216, v229, s[54:55]
	v_max3_f32 v168, v168, v223, v224
	v_cndmask_b32_e64 v225, v216, v230, s[56:57]
	v_cndmask_b32_e64 v226, v216, v231, s[58:59]
	v_max3_f32 v168, v168, v225, v226
	v_max3_f32 v168, v168, v227, v228
	v_cndmask_b32_e64 v229, v216, v234, s[64:65]
	v_cndmask_b32_e64 v230, v216, v235, s[66:67]
	v_max3_f32 v168, v168, v229, v230
	v_cndmask_b32_e64 v231, v216, v236, s[68:69]
	v_max3_f32 v168, v168, v231, v232
	v_cndmask_b32_e64 v234, v216, v239, s[74:75]
	v_max3_f32 v168, v168, v233, v234
	v_cndmask_b32_e64 v235, v216, v240, s[76:77]
	v_cndmask_b32_e64 v236, v216, v241, s[78:79]
	v_max3_f32 v168, v168, v235, v236
	v_max3_f32 v168, v168, v237, v238
	v_cndmask_b32_e64 v239, v216, v244, s[84:85]
	v_cndmask_b32_e64 v240, v216, v245, s[86:87]
	v_max3_f32 v168, v168, v239, v240
	v_cndmask_b32_e64 v241, v216, v246, s[88:89]
	v_max3_f32 v168, v168, v241, v242
	v_cndmask_b32_e64 v244, v216, v249, s[94:95]
	v_max3_f32 v168, v168, v243, v244
	v_cndmask_b32_e64 v245, v216, v198, s[96:97]
	v_cndmask_b32_e64 v246, v216, v199, s[2:3]
	v_max3_f32 v168, v168, v245, v246
	v_max3_f32 v168, v168, v247, v248
	v_cndmask_b32_e64 v249, v216, v164, s[8:9]
	v_cndmask_b32_e64 v252, v216, v165, s[10:11]
	v_max3_f32 v164, v168, v249, v252
	v_cndmask_b32_e64 v168, v216, v166, s[12:13]
	v_cndmask_b32_e64 v217, v216, v167, s[14:15]
	v_max3_f32 v164, v164, v168, v217
	v_mov_b32_e32 v166, v164
	s_nop 1
	v_permlane16_swap_b32_e32 v166, v164
	s_waitcnt vmcnt(0)
; __device__ __forceinline__ unsigned pk2(float lo, float hi) { f32x2_m v = {lo, hi}; bf16x2_m b = __builtin_convertvector(v, bf16x2_m); return __builtin_bit_cast(unsigned, b); }
; __device__ __forceinline__ void swa_phase(const Ctx& C, const bf16* PROJ, const float* sinks, bf16* YSWA) {
;     ...
;             mx = fmaxf(mx, __shfl_xor(mx, 16)); mx = fmaxf(mx, __shfl_xor(mx, 32)); mx = fmaxf(mx, sink2);
;             float sum = 0.f;
; #pragma unroll
;             for (int j = 0; j < 9; ++j)
; #pragma unroll
;                 for (int r = 0; r < 4; ++r) { const float e = __builtin_amdgcn_exp2f(s[j][r] - mx); s[j][r] = e; sum += e; }
;             sum += __shfl_xor(sum, 16); sum += __shfl_xor(sum, 32); sum += __builtin_amdgcn_exp2f(sink2 - mx);
;             const float inv = 1.0f / sum;
;             unsigned pw[10][2];
; #pragma unroll
;             for (int j = 0; j < 9; ++j) { pw[j][0] = pk2(s[j][0] * inv, s[j][1] * inv); pw[j][1] = pk2(s[j][2] * inv, s[j][3] * inv); }
	v_mul_f32_e32 v165, 0x3fb8aa3b, v3
	v_mfma_f32_16x16x32_bf16 v[4:7], v[4:7], v[80:83], 0
	s_waitcnt lgkmcnt(0)
	v_max_f32_e32 v164, v164, v166
	v_mov_b32_e32 v166, v164
	s_nop 1
	v_permlane32_swap_b32_e32 v166, v164
	v_mfma_f32_16x16x32_bf16 v[4:7], v[8:11], v[76:79], v[4:7]
	s_waitcnt lgkmcnt(0)
	v_max3_f32 v207, v164, v166, v165
	v_sub_f32_e32 v164, v169, v207
	v_sub_f32_e32 v169, v223, v207
	v_exp_f32_e32 v198, v169
	v_sub_f32_e32 v169, v224, v207
	v_exp_f32_e32 v199, v169
	v_sub_f32_e32 v169, v225, v207
	v_exp_f32_e32 v200, v169
	v_sub_f32_e32 v169, v226, v207
	v_exp_f32_e32 v201, v169
	v_sub_f32_e32 v169, v227, v207
	v_sub_f32_e32 v167, v222, v207
	v_exp_f32_e32 v222, v169
	v_sub_f32_e32 v169, v228, v207
	v_exp_f32_e32 v223, v169
	v_sub_f32_e32 v169, v229, v207
	v_exp_f32_e32 v224, v169
	v_sub_f32_e32 v169, v230, v207
	v_exp_f32_e32 v225, v169
	v_sub_f32_e32 v169, v231, v207
	v_exp_f32_e32 v226, v169
	v_sub_f32_e32 v169, v232, v207
	v_exp_f32_e32 v227, v169
	v_sub_f32_e32 v169, v233, v207
	v_exp_f32_e32 v228, v169
	v_sub_f32_e32 v169, v234, v207
	v_exp_f32_e32 v229, v169
	v_sub_f32_e32 v169, v235, v207
	v_exp_f32_e32 v230, v169
	v_sub_f32_e32 v169, v236, v207
	v_exp_f32_e32 v231, v169
	v_sub_f32_e32 v169, v237, v207
	v_exp_f32_e32 v232, v169
	v_sub_f32_e32 v169, v238, v207
	v_exp_f32_e32 v233, v169
	v_sub_f32_e32 v169, v239, v207
	v_exp_f32_e32 v234, v169
	v_sub_f32_e32 v169, v240, v207
	v_exp_f32_e32 v235, v169
	v_sub_f32_e32 v169, v241, v207
	v_sub_f32_e32 v0, v0, v207
	v_exp_f32_e32 v236, v169
	v_sub_f32_e32 v169, v242, v207
	v_exp_f32_e32 v0, v0
	v_sub_f32_e32 v1, v1, v207
	v_exp_f32_e32 v237, v169
	v_sub_f32_e32 v169, v243, v207
	v_exp_f32_e32 v1, v1
	v_exp_f32_e32 v238, v169
	v_sub_f32_e32 v169, v244, v207
	v_exp_f32_e32 v164, v164
	v_sub_f32_e32 v165, v170, v207
	v_exp_f32_e32 v239, v169
	v_sub_f32_e32 v169, v245, v207
	v_sub_f32_e32 v168, v168, v207
	v_exp_f32_e32 v165, v165
	v_sub_f32_e32 v166, v171, v207
	v_exp_f32_e32 v240, v169
	v_sub_f32_e32 v169, v246, v207
	v_exp_f32_e32 v246, v168
	v_sub_f32_e32 v168, v217, v207
	v_exp_f32_e32 v166, v166
	v_exp_f32_e32 v241, v169
	v_sub_f32_e32 v169, v247, v207
	v_exp_f32_e32 v247, v168
	v_add_f32_e32 v168, 0, v0
	v_exp_f32_e32 v167, v167
	v_add_f32_e32 v168, v1, v168
	v_add_f32_e32 v168, v164, v168
	v_add_f32_e32 v168, v165, v168
	v_add_f32_e32 v168, v166, v168
	v_add_f32_e32 v168, v167, v168
	v_add_f32_e32 v168, v198, v168
	v_add_f32_e32 v168, v199, v168
	v_add_f32_e32 v168, v200, v168
	v_add_f32_e32 v168, v201, v168
	v_add_f32_e32 v168, v222, v168
	v_add_f32_e32 v168, v223, v168
	v_add_f32_e32 v168, v224, v168
	v_add_f32_e32 v168, v225, v168
	v_add_f32_e32 v168, v226, v168
	v_add_f32_e32 v168, v227, v168
	v_add_f32_e32 v168, v228, v168
	v_add_f32_e32 v168, v229, v168
	v_add_f32_e32 v168, v230, v168
	v_add_f32_e32 v168, v231, v168
	v_add_f32_e32 v168, v232, v168
	v_add_f32_e32 v168, v233, v168
	v_add_f32_e32 v168, v234, v168
	v_add_f32_e32 v168, v235, v168
	v_add_f32_e32 v168, v236, v168
	v_add_f32_e32 v168, v237, v168
	v_exp_f32_e32 v242, v169
	v_sub_f32_e32 v169, v248, v207
	v_add_f32_e32 v168, v238, v168
	v_exp_f32_e32 v243, v169
	v_sub_f32_e32 v169, v249, v207
	v_add_f32_e32 v168, v239, v168
	v_exp_f32_e32 v244, v169
	v_sub_f32_e32 v169, v252, v207
	v_add_f32_e32 v168, v240, v168
	v_exp_f32_e32 v245, v169
	v_add_f32_e32 v168, v241, v168
	v_add_f32_e32 v168, v242, v168
	v_add_f32_e32 v168, v243, v168
	v_add_f32_e32 v168, v244, v168
	v_add_f32_e32 v168, v245, v168
	v_add_f32_e32 v168, v246, v168
	v_add_f32_e32 v168, v247, v168
	v_mov_b32_e32 v169, v168
	s_nop 1
	v_permlane16_swap_b32_e32 v169, v168
	v_fma_f32 v3, v3, s23, -v207
	v_exp_f32_e32 v3, v3
	v_mfma_f32_16x16x32_bf16 v[8:11], v[12:15], v[80:83], 0
	s_waitcnt lgkmcnt(0)
	v_add_f32_e32 v168, v168, v169
	v_mov_b32_e32 v169, v168
	s_nop 1
	v_permlane32_swap_b32_e32 v169, v168
	v_mfma_f32_16x16x32_bf16 v[12:15], v[20:23], v[80:83], 0
	s_waitcnt lgkmcnt(0)
	v_add_f32_e32 v168, v168, v169
	v_add_f32_e32 v3, v3, v168
	v_div_scale_f32 v168, s[20:21], v3, v3, 1.0
	v_rcp_f32_e32 v169, v168
	v_mfma_f32_16x16x32_bf16 v[8:11], v[16:19], v[76:79], v[8:11]
	v_fma_f32 v170, -v168, v169, 1.0
	v_fmac_f32_e32 v169, v170, v169
	v_div_scale_f32 v170, vcc, 1.0, v3, 1.0
	v_mul_f32_e32 v171, v170, v169
	v_fma_f32 v207, -v168, v171, v170
	v_fmac_f32_e32 v171, v207, v169
	v_fma_f32 v168, -v168, v171, v170
	v_div_fmas_f32 v168, v168, v169, v171
	v_div_fixup_f32 v248, v168, v3, 1.0
	v_pk_mul_f32 v[0:1], v[0:1], v[248:249] op_sel_hi:[1,0]
	v_mov_b32_e32 v3, v2
	v_cvt_pk_bf16_f32 v168, v0, v1
	v_pk_mul_f32 v[0:1], v[164:165], v[248:249] op_sel_hi:[1,0]
	v_mfma_f32_16x16x32_bf16 v[16:19], v[28:31], v[80:83], 0
	v_cvt_pk_bf16_f32 v169, v0, v1
	v_pk_mul_f32 v[0:1], v[166:167], v[248:249] op_sel_hi:[1,0]
	s_nop 0
	v_cvt_pk_bf16_f32 v170, v0, v1
	v_pk_mul_f32 v[0:1], v[198:199], v[248:249] op_sel_hi:[1,0]
	v_mfma_f32_16x16x32_bf16 v[12:15], v[24:27], v[76:79], v[12:15]
	v_cvt_pk_bf16_f32 v171, v0, v1
	v_pk_mul_f32 v[0:1], v[200:201], v[248:249] op_sel_hi:[1,0]
	s_nop 0
	v_cvt_pk_bf16_f32 v198, v0, v1
	v_pk_mul_f32 v[0:1], v[222:223], v[248:249] op_sel_hi:[1,0]
	v_mfma_f32_16x16x32_bf16 v[20:23], v[36:39], v[80:83], 0
	v_cvt_pk_bf16_f32 v199, v0, v1
	v_pk_mul_f32 v[0:1], v[224:225], v[248:249] op_sel_hi:[1,0]
	s_nop 0
	v_cvt_pk_bf16_f32 v200, v0, v1
	v_pk_mul_f32 v[0:1], v[226:227], v[248:249] op_sel_hi:[1,0]
	v_pk_mul_f32 v[226:227], v[246:247], v[248:249] op_sel_hi:[1,0]
	v_cvt_pk_bf16_f32 v201, v0, v1
	v_pk_mul_f32 v[0:1], v[228:229], v[248:249] op_sel_hi:[1,0]
	v_mfma_f32_16x16x32_bf16 v[16:19], v[32:35], v[76:79], v[16:19]
	v_cvt_pk_bf16_f32 v222, v0, v1
; #define GAS __attribute__((address_space(1)))
; #define LAS __attribute__((address_space(3)))
; __device__ __forceinline__ unsigned pk2(float lo, float hi) { f32x2_m v = {lo, hi}; bf16x2_m b = __builtin_convertvector(v, bf16x2_m); return __builtin_bit_cast(unsigned, b); }
; #define MFMA16(a, b, c) __builtin_amdgcn_mfma_f32_16x16x32_bf16(a, b, c, 0, 0, 0)
; __device__ __forceinline__ void swa_phase(const Ctx& C, const bf16* PROJ, const float* sinks, bf16* YSWA) {
;     ...
;             const int qr = 16 * w + c16; float mx = -INFINITY;
; #pragma unroll
;             for (int j = 0; j < 9; ++j)
; #pragma unroll
;                 for (int r = 0; r < 4; ++r) { const int kr = 16 * w - 128 + 16 * j + 4 * g4 + r, diff = qr - kr; const bool ok = diff >= 0 && diff < 128 && (128 * n + kr) >= 0;
;                     s[j][r] = ok ? s[j][r] : -INFINITY; mx = fmaxf(mx, s[j][r]); }
;             mx = fmaxf(mx, __shfl_xor(mx, 16)); mx = fmaxf(mx, __shfl_xor(mx, 32)); mx = fmaxf(mx, sink2);
;     ...
;             for (int j = 0; j < 9; ++j) { pw[j][0] = pk2(s[j][0] * inv, s[j][1] * inv); pw[j][1] = pk2(s[j][2] * inv, s[j][3] * inv); }
;             pw[9][0] = 0u; pw[9][1] = 0u;
;             f32x4 o[4];
; #pragma unroll
;             for (int dt = 0; dt < 4; ++dt) o[dt] = (f32x4){0.f, 0.f, 0.f, 0.f};
; #pragma unroll
;             for (int sI = 0; sI < 5; ++sI) {
;                 const v4u pb = {pw[2 * sI][0], pw[2 * sI][1], pw[2 * sI + 1][0], pw[2 * sI + 1][1]};
;                 const int kkA = 16 * w + 32 * sI + 4 * g4; int kkB = kkA + 16; if (kkB > 252) kkB = 252;
; #pragma unroll
;                 for (int dt = 0; dt < 4; ++dt) { const LAS bf16* vp = vt + (16 * dt + c16) * 264;
;                     const v2u va = *(const LAS v2u*)(vp + kkA), vb = *(const LAS v2u*)(vp + kkB);
;                     const v4u av = {va.x, va.y, vb.x, vb.y};
;                     o[dt] = MFMA16(__builtin_bit_cast(bf16x8, av), __builtin_bit_cast(bf16x8, pb), o[dt]); }
;             }
;             bf16* op = YSWA + (size_t)(q0 + c16) * 768 + 64 * h + 4 * g4;
; #pragma unroll
;             for (int dt = 0; dt < 4; ++dt) { v2u wv; wv.x = pk2(o[dt][0], o[dt][1]); wv.y = pk2(o[dt][2], o[dt][3]); *(GAS v2u*)(op + 16 * dt) = wv; }
	v_pk_mul_f32 v[0:1], v[230:231], v[248:249] op_sel_hi:[1,0]
	s_nop 0
	v_cvt_pk_bf16_f32 v223, v0, v1
	v_pk_mul_f32 v[0:1], v[232:233], v[248:249] op_sel_hi:[1,0]
	v_mfma_f32_16x16x32_bf16 v[230:233], v[96:99], v[168:171], 0
	v_cvt_pk_bf16_f32 v224, v0, v1
	v_pk_mul_f32 v[0:1], v[234:235], v[248:249] op_sel_hi:[1,0]
	s_nop 0
	v_cvt_pk_bf16_f32 v225, v0, v1
	v_pk_mul_f32 v[0:1], v[236:237], v[248:249] op_sel_hi:[1,0]
	v_mfma_f32_16x16x32_bf16 v[234:237], v[100:103], v[168:171], 0
	v_cvt_pk_bf16_f32 v164, v0, v1
	v_pk_mul_f32 v[0:1], v[238:239], v[248:249] op_sel_hi:[1,0]
	s_nop 0
	v_cvt_pk_bf16_f32 v165, v0, v1
	v_pk_mul_f32 v[0:1], v[240:241], v[248:249] op_sel_hi:[1,0]
	v_mfma_f32_16x16x32_bf16 v[230:233], v[112:115], v[198:201], v[230:233]
	v_cvt_pk_bf16_f32 v166, v0, v1
	v_pk_mul_f32 v[0:1], v[242:243], v[248:249] op_sel_hi:[1,0]
	s_nop 0
	v_cvt_pk_bf16_f32 v167, v0, v1
	v_pk_mul_f32 v[0:1], v[244:245], v[248:249] op_sel_hi:[1,0]
	v_mfma_f32_16x16x32_bf16 v[234:237], v[116:119], v[198:201], v[234:237]
	v_cvt_pk_bf16_f32 v0, v0, v1
	v_cvt_pk_bf16_f32 v1, v226, v227
	v_mfma_f32_16x16x32_bf16 v[226:229], v[92:95], v[168:171], 0
	v_mfma_f32_16x16x32_bf16 v[168:171], v[104:107], v[168:171], 0
	v_mfma_f32_16x16x32_bf16 v[226:229], v[108:111], v[198:201], v[226:229]
	v_mfma_f32_16x16x32_bf16 v[168:171], v[120:123], v[198:201], v[168:171]
	v_mfma_f32_16x16x32_bf16 v[198:201], v[124:127], v[222:225], v[226:229]
	v_mfma_f32_16x16x32_bf16 v[226:229], v[128:131], v[222:225], v[230:233]
	v_mfma_f32_16x16x32_bf16 v[230:233], v[132:135], v[222:225], v[234:237]
	v_mfma_f32_16x16x32_bf16 v[168:171], v[136:139], v[222:225], v[168:171]
	v_mfma_f32_16x16x32_bf16 v[198:201], v[140:143], v[164:167], v[198:201]
	v_mfma_f32_16x16x32_bf16 v[222:225], v[144:147], v[164:167], v[226:229]
	v_mfma_f32_16x16x32_bf16 v[226:229], v[148:151], v[164:167], v[230:233]
	v_mfma_f32_16x16x32_bf16 v[164:167], v[152:155], v[164:167], v[168:171]
	v_mfma_f32_16x16x32_bf16 v[168:171], v[84:87], v[0:3], v[198:201]
	v_mfma_f32_16x16x32_bf16 v[198:201], v[156:159], v[0:3], v[222:225]
	v_mfma_f32_16x16x32_bf16 v[222:225], v[88:91], v[0:3], v[226:229]
	s_nop 5
	v_cvt_pk_bf16_f32 v168, v168, v169
	v_cvt_pk_bf16_f32 v169, v170, v171
	v_mfma_f32_16x16x32_bf16 v[164:167], v[160:163], v[0:3], v[164:167]
	v_lshl_add_u64 v[0:1], v[180:181], 0, s[26:27]
	global_store_dwordx2 v[0:1], v[168:169], off
	v_cvt_pk_bf16_f32 v168, v198, v199
	v_cvt_pk_bf16_f32 v169, v200, v201
	global_store_dwordx2 v[0:1], v[168:169], off offset:32
	v_cvt_pk_bf16_f32 v168, v222, v223
	v_cvt_pk_bf16_f32 v169, v224, v225
	s_nop 0
	v_cvt_pk_bf16_f32 v164, v164, v165
	v_cvt_pk_bf16_f32 v165, v166, v167
	global_store_dwordx2 v[0:1], v[168:169], off offset:64
	global_store_dwordx2 v[0:1], v[164:165], off offset:96
	global_load_dword v3, v221, s[36:37] offset:8
	v_cndmask_b32_e64 v0, v216, v4, s[40:41]
	v_cndmask_b32_e64 v1, v216, v5, s[42:43]
	v_max3_f32 v4, v0, s22, v1
	v_cndmask_b32_e64 v5, v216, v6, s[44:45]
	v_cndmask_b32_e64 v6, v216, v7, s[46:47]
	v_mfma_f32_16x16x32_bf16 v[24:27], v[44:47], v[80:83], 0
	v_max3_f32 v4, v4, v5, v6
	v_cndmask_b32_e64 v7, v216, v8, s[48:49]
	v_cndmask_b32_e64 v8, v216, v9, s[50:51]
	v_max3_f32 v4, v4, v7, v8
	v_cndmask_b32_e64 v9, v216, v10, s[52:53]
	v_cndmask_b32_e64 v10, v216, v11, s[54:55]
	v_mfma_f32_16x16x32_bf16 v[20:23], v[40:43], v[76:79], v[20:23]
	v_max3_f32 v4, v4, v9, v10
	v_cndmask_b32_e64 v11, v216, v12, s[56:57]
	v_cndmask_b32_e64 v40, v216, v13, s[58:59]
	v_mfma_f32_16x16x32_bf16 v[28:31], v[60:63], v[80:83], 0
	v_max3_f32 v4, v4, v11, v40
	v_cndmask_b32_e64 v41, v216, v14, s[60:61]
	v_cndmask_b32_e64 v42, v216, v15, s[62:63]
	v_mfma_f32_16x16x32_bf16 v[24:27], v[48:51], v[76:79], v[24:27]
	v_max3_f32 v4, v4, v41, v42
	v_cndmask_b32_e64 v43, v216, v16, s[64:65]
	v_cndmask_b32_e64 v44, v216, v17, s[66:67]
	v_mfma_f32_16x16x32_bf16 v[32:35], v[64:67], v[80:83], 0
	v_max3_f32 v4, v4, v43, v44
	v_cndmask_b32_e64 v45, v216, v18, s[68:69]
	v_cndmask_b32_e64 v46, v216, v19, s[70:71]
	v_mfma_f32_16x16x32_bf16 v[28:31], v[52:55], v[76:79], v[28:31]
	v_max3_f32 v4, v4, v45, v46
	v_cndmask_b32_e64 v47, v216, v20, s[72:73]
	v_cndmask_b32_e64 v48, v216, v21, s[74:75]
	v_mfma_f32_16x16x32_bf16 v[36:39], v[72:75], v[80:83], 0
	v_max3_f32 v4, v4, v47, v48
	v_cndmask_b32_e64 v49, v216, v22, s[76:77]
	v_cndmask_b32_e64 v50, v216, v23, s[78:79]
	v_mfma_f32_16x16x32_bf16 v[32:35], v[56:59], v[76:79], v[32:35]
	v_max3_f32 v4, v4, v49, v50
	v_cndmask_b32_e64 v51, v216, v24, s[80:81]
	v_cndmask_b32_e64 v52, v216, v25, s[82:83]
	v_max3_f32 v4, v4, v51, v52
	v_cndmask_b32_e64 v53, v216, v26, s[84:85]
	v_cndmask_b32_e64 v54, v216, v27, s[86:87]
	v_mfma_f32_16x16x32_bf16 v[36:39], v[68:71], v[76:79], v[36:39]
	v_max3_f32 v4, v4, v53, v54
	v_cndmask_b32_e64 v55, v216, v28, s[88:89]
	v_cndmask_b32_e64 v56, v216, v29, s[90:91]
	v_max3_f32 v4, v4, v55, v56
	v_cndmask_b32_e64 v57, v216, v30, s[92:93]
	v_cndmask_b32_e64 v58, v216, v31, s[94:95]
	v_max3_f32 v4, v4, v57, v58
	v_cndmask_b32_e64 v59, v216, v32, s[96:97]
	v_cndmask_b32_e64 v60, v216, v33, s[2:3]
	v_max3_f32 v4, v4, v59, v60
	v_cndmask_b32_e64 v61, v216, v34, s[4:5]
	v_cndmask_b32_e64 v62, v216, v35, s[6:7]
	v_max3_f32 v4, v4, v61, v62
	v_cndmask_b32_e64 v63, v216, v36, s[8:9]
	v_cndmask_b32_e64 v64, v216, v37, s[10:11]
	v_max3_f32 v4, v4, v63, v64
	v_cndmask_b32_e64 v65, v216, v38, s[12:13]
	v_cndmask_b32_e64 v66, v216, v39, s[14:15]
	v_max3_f32 v4, v4, v65, v66
	v_mov_b32_e32 v13, v4
	s_nop 1
	v_permlane16_swap_b32_e32 v13, v4
	s_waitcnt lgkmcnt(0)
	v_max_f32_e32 v4, v4, v13
	v_mov_b32_e32 v13, v4
	s_nop 1
	v_permlane32_swap_b32_e32 v13, v4
	s_waitcnt vmcnt(0)
; __device__ __forceinline__ void swa_phase(const Ctx& C, const bf16* PROJ, const float* sinks, bf16* YSWA) {
;     ...
;             mx = fmaxf(mx, __shfl_xor(mx, 16)); mx = fmaxf(mx, __shfl_xor(mx, 32)); mx = fmaxf(mx, sink2);
;             float sum = 0.f;
; #pragma unroll
;             for (int j = 0; j < 9; ++j)
; #pragma unroll
;                 for (int r = 0; r < 4; ++r) { const float e = __builtin_amdgcn_exp2f(s[j][r] - mx); s[j][r] = e; sum += e; }
;             sum += __shfl_xor(sum, 16); sum += __shfl_xor(sum, 32); sum += __builtin_amdgcn_exp2f(sink2 - mx);
	v_mul_f32_e32 v12, 0x3fb8aa3b, v3
	s_waitcnt lgkmcnt(0)
	v_max3_f32 v67, v4, v13, v12
	v_sub_f32_e32 v4, v5, v67
	v_sub_f32_e32 v5, v6, v67
	v_sub_f32_e32 v6, v7, v67
	v_sub_f32_e32 v7, v8, v67
	v_sub_f32_e32 v8, v9, v67
	v_exp_f32_e32 v12, v8
	v_sub_f32_e32 v8, v10, v67
	v_exp_f32_e32 v13, v8
	v_sub_f32_e32 v8, v11, v67
	v_exp_f32_e32 v14, v8
	v_sub_f32_e32 v8, v40, v67
	v_exp_f32_e32 v15, v8
	v_sub_f32_e32 v8, v41, v67
	v_exp_f32_e32 v16, v8
	v_sub_f32_e32 v8, v42, v67
	v_exp_f32_e32 v17, v8
	v_sub_f32_e32 v8, v43, v67
	v_exp_f32_e32 v18, v8
	v_sub_f32_e32 v8, v44, v67
	v_exp_f32_e32 v19, v8
	v_sub_f32_e32 v8, v45, v67
	v_exp_f32_e32 v20, v8
	v_sub_f32_e32 v8, v46, v67
	v_exp_f32_e32 v21, v8
	v_sub_f32_e32 v8, v47, v67
	v_exp_f32_e32 v22, v8
	v_sub_f32_e32 v8, v48, v67
	v_exp_f32_e32 v23, v8
	v_sub_f32_e32 v8, v49, v67
	v_exp_f32_e32 v24, v8
	v_sub_f32_e32 v8, v50, v67
	v_exp_f32_e32 v25, v8
	v_sub_f32_e32 v8, v51, v67
	v_exp_f32_e32 v26, v8
	v_sub_f32_e32 v8, v52, v67
	v_exp_f32_e32 v27, v8
	v_sub_f32_e32 v8, v53, v67
	v_exp_f32_e32 v28, v8
	v_sub_f32_e32 v8, v54, v67
	v_exp_f32_e32 v29, v8
	v_sub_f32_e32 v8, v55, v67
	v_exp_f32_e32 v30, v8
	v_sub_f32_e32 v8, v56, v67
	v_exp_f32_e32 v31, v8
	v_sub_f32_e32 v8, v57, v67
	v_exp_f32_e32 v32, v8
	v_sub_f32_e32 v8, v58, v67
	v_exp_f32_e32 v33, v8
	v_sub_f32_e32 v8, v59, v67
	v_exp_f32_e32 v34, v8
	v_sub_f32_e32 v8, v60, v67
	v_exp_f32_e32 v35, v8
	v_sub_f32_e32 v8, v61, v67
	v_sub_f32_e32 v0, v0, v67
	v_exp_f32_e32 v36, v8
	v_sub_f32_e32 v8, v62, v67
	v_exp_f32_e32 v0, v0
	v_sub_f32_e32 v1, v1, v67
	v_exp_f32_e32 v37, v8
	v_sub_f32_e32 v8, v63, v67
	v_exp_f32_e32 v1, v1
	v_exp_f32_e32 v38, v8
	v_sub_f32_e32 v8, v64, v67
	v_exp_f32_e32 v4, v4
	v_exp_f32_e32 v39, v8
	v_sub_f32_e32 v8, v65, v67
	v_exp_f32_e32 v5, v5
	v_exp_f32_e32 v40, v8
	v_sub_f32_e32 v8, v66, v67
	v_exp_f32_e32 v6, v6
	v_exp_f32_e32 v41, v8
	v_add_f32_e32 v8, 0, v0
	v_exp_f32_e32 v7, v7
	v_add_f32_e32 v8, v1, v8
	v_add_f32_e32 v8, v4, v8
	v_add_f32_e32 v8, v5, v8
	v_add_f32_e32 v8, v6, v8
	v_add_f32_e32 v8, v7, v8
	v_add_f32_e32 v8, v12, v8
	v_add_f32_e32 v8, v13, v8
	v_add_f32_e32 v8, v14, v8
	v_add_f32_e32 v8, v15, v8
	v_add_f32_e32 v8, v16, v8
	v_add_f32_e32 v8, v17, v8
	v_add_f32_e32 v8, v18, v8
	v_add_f32_e32 v8, v19, v8
	v_add_f32_e32 v8, v20, v8
	v_add_f32_e32 v8, v21, v8
	v_add_f32_e32 v8, v22, v8
	v_add_f32_e32 v8, v23, v8
	v_add_f32_e32 v8, v24, v8
	v_add_f32_e32 v8, v25, v8
	v_add_f32_e32 v8, v26, v8
	v_add_f32_e32 v8, v27, v8
	v_add_f32_e32 v8, v28, v8
	v_add_f32_e32 v8, v29, v8
	v_add_f32_e32 v8, v30, v8
	v_add_f32_e32 v8, v31, v8
	v_add_f32_e32 v8, v32, v8
	v_add_f32_e32 v8, v33, v8
	v_add_f32_e32 v8, v34, v8
	v_add_f32_e32 v8, v35, v8
	v_add_f32_e32 v8, v36, v8
	v_add_f32_e32 v8, v37, v8
	v_add_f32_e32 v8, v38, v8
	v_add_f32_e32 v8, v39, v8
	v_add_f32_e32 v8, v40, v8
	v_add_f32_e32 v8, v41, v8
	v_mov_b32_e32 v9, v8
	s_nop 1
	v_permlane16_swap_b32_e32 v9, v8
	v_fma_f32 v3, v3, s23, -v67
	v_exp_f32_e32 v3, v3
	s_waitcnt lgkmcnt(0)
	v_add_f32_e32 v8, v8, v9
	v_mov_b32_e32 v9, v8
	s_nop 1
	v_permlane32_swap_b32_e32 v9, v8
	s_waitcnt lgkmcnt(0)
; #define GAS __attribute__((address_space(1)))
; #define LAS __attribute__((address_space(3)))
; __device__ __forceinline__ unsigned pk2(float lo, float hi) { f32x2_m v = {lo, hi}; bf16x2_m b = __builtin_convertvector(v, bf16x2_m); return __builtin_bit_cast(unsigned, b); }
; #define MFMA16(a, b, c) __builtin_amdgcn_mfma_f32_16x16x32_bf16(a, b, c, 0, 0, 0)
; __device__ __forceinline__ void swa_phase(const Ctx& C, const bf16* PROJ, const float* sinks, bf16* YSWA) {
;     ...
;     for (int u = C.vcu; u < 512; u += C.G) {
;     ...
;             sum += __shfl_xor(sum, 16); sum += __shfl_xor(sum, 32); sum += __builtin_amdgcn_exp2f(sink2 - mx);
;             const float inv = 1.0f / sum;
;             unsigned pw[10][2];
; #pragma unroll
;             for (int j = 0; j < 9; ++j) { pw[j][0] = pk2(s[j][0] * inv, s[j][1] * inv); pw[j][1] = pk2(s[j][2] * inv, s[j][3] * inv); }
;             pw[9][0] = 0u; pw[9][1] = 0u;
;             f32x4 o[4];
; #pragma unroll
;             for (int dt = 0; dt < 4; ++dt) o[dt] = (f32x4){0.f, 0.f, 0.f, 0.f};
; #pragma unroll
;             for (int sI = 0; sI < 5; ++sI) {
;                 const v4u pb = {pw[2 * sI][0], pw[2 * sI][1], pw[2 * sI + 1][0], pw[2 * sI + 1][1]};
;                 const int kkA = 16 * w + 32 * sI + 4 * g4; int kkB = kkA + 16; if (kkB > 252) kkB = 252;
; #pragma unroll
;                 for (int dt = 0; dt < 4; ++dt) { const LAS bf16* vp = vt + (16 * dt + c16) * 264;
;                     const v2u va = *(const LAS v2u*)(vp + kkA), vb = *(const LAS v2u*)(vp + kkB);
;                     const v4u av = {va.x, va.y, vb.x, vb.y};
;                     o[dt] = MFMA16(__builtin_bit_cast(bf16x8, av), __builtin_bit_cast(bf16x8, pb), o[dt]); }
;             }
;             bf16* op = YSWA + (size_t)(q0 + c16) * 768 + 64 * h + 4 * g4;
; #pragma unroll
;             for (int dt = 0; dt < 4; ++dt) { v2u wv; wv.x = pk2(o[dt][0], o[dt][1]); wv.y = pk2(o[dt][2], o[dt][3]); *(GAS v2u*)(op + 16 * dt) = wv; }
	v_add_f32_e32 v8, v8, v9
	v_add_f32_e32 v3, v3, v8
	v_div_scale_f32 v8, s[20:21], v3, v3, 1.0
	v_rcp_f32_e32 v9, v8
	s_add_i32 s20, s19, 0x100
	s_cmpk_lt_i32 s19, 0x100
	s_mov_b32 s19, s20
	v_fma_f32 v10, -v8, v9, 1.0
	v_fmac_f32_e32 v9, v10, v9
	v_div_scale_f32 v10, vcc, 1.0, v3, 1.0
	v_mul_f32_e32 v11, v10, v9
	v_fma_f32 v42, -v8, v11, v10
	v_fmac_f32_e32 v11, v42, v9
	v_fma_f32 v8, -v8, v11, v10
	v_div_fmas_f32 v8, v8, v9, v11
	v_div_fixup_f32 v42, v8, v3, 1.0
	v_pk_mul_f32 v[0:1], v[0:1], v[42:43] op_sel_hi:[1,0]
	v_mov_b32_e32 v3, v2
	v_cvt_pk_bf16_f32 v8, v0, v1
	v_pk_mul_f32 v[0:1], v[4:5], v[42:43] op_sel_hi:[1,0]
	s_nop 0
	v_cvt_pk_bf16_f32 v9, v0, v1
	v_pk_mul_f32 v[0:1], v[6:7], v[42:43] op_sel_hi:[1,0]
	s_nop 0
	v_cvt_pk_bf16_f32 v10, v0, v1
	v_pk_mul_f32 v[0:1], v[12:13], v[42:43] op_sel_hi:[1,0]
	s_nop 0
	v_cvt_pk_bf16_f32 v11, v0, v1
	v_pk_mul_f32 v[0:1], v[14:15], v[42:43] op_sel_hi:[1,0]
	s_nop 0
	v_cvt_pk_bf16_f32 v12, v0, v1
	v_pk_mul_f32 v[0:1], v[16:17], v[42:43] op_sel_hi:[1,0]
	s_nop 0
	v_cvt_pk_bf16_f32 v13, v0, v1
	v_pk_mul_f32 v[0:1], v[18:19], v[42:43] op_sel_hi:[1,0]
	s_nop 0
	v_cvt_pk_bf16_f32 v14, v0, v1
	v_pk_mul_f32 v[0:1], v[20:21], v[42:43] op_sel_hi:[1,0]
	v_pk_mul_f32 v[20:21], v[40:41], v[42:43] op_sel_hi:[1,0]
	v_cvt_pk_bf16_f32 v15, v0, v1
	v_pk_mul_f32 v[0:1], v[22:23], v[42:43] op_sel_hi:[1,0]
	s_nop 0
	v_cvt_pk_bf16_f32 v16, v0, v1
	v_pk_mul_f32 v[0:1], v[24:25], v[42:43] op_sel_hi:[1,0]
	s_nop 0
	v_cvt_pk_bf16_f32 v17, v0, v1
	v_pk_mul_f32 v[0:1], v[26:27], v[42:43] op_sel_hi:[1,0]
	v_mfma_f32_16x16x32_bf16 v[24:27], v[96:99], v[8:11], 0
	v_cvt_pk_bf16_f32 v18, v0, v1
	v_pk_mul_f32 v[0:1], v[28:29], v[42:43] op_sel_hi:[1,0]
	s_nop 0
	v_cvt_pk_bf16_f32 v19, v0, v1
	v_pk_mul_f32 v[0:1], v[30:31], v[42:43] op_sel_hi:[1,0]
	v_mfma_f32_16x16x32_bf16 v[28:31], v[100:103], v[8:11], 0
	v_cvt_pk_bf16_f32 v4, v0, v1
	v_pk_mul_f32 v[0:1], v[32:33], v[42:43] op_sel_hi:[1,0]
	s_nop 0
	v_cvt_pk_bf16_f32 v5, v0, v1
	v_pk_mul_f32 v[0:1], v[34:35], v[42:43] op_sel_hi:[1,0]
	v_mfma_f32_16x16x32_bf16 v[24:27], v[112:115], v[12:15], v[24:27]
	v_cvt_pk_bf16_f32 v6, v0, v1
	v_pk_mul_f32 v[0:1], v[36:37], v[42:43] op_sel_hi:[1,0]
	s_nop 0
	v_cvt_pk_bf16_f32 v7, v0, v1
	v_pk_mul_f32 v[0:1], v[38:39], v[42:43] op_sel_hi:[1,0]
	v_mfma_f32_16x16x32_bf16 v[28:31], v[116:119], v[12:15], v[28:31]
	v_cvt_pk_bf16_f32 v0, v0, v1
	v_cvt_pk_bf16_f32 v1, v20, v21
	v_mfma_f32_16x16x32_bf16 v[20:23], v[92:95], v[8:11], 0
	v_mfma_f32_16x16x32_bf16 v[8:11], v[104:107], v[8:11], 0
	v_mfma_f32_16x16x32_bf16 v[20:23], v[108:111], v[12:15], v[20:23]
	v_mfma_f32_16x16x32_bf16 v[8:11], v[120:123], v[12:15], v[8:11]
	v_mfma_f32_16x16x32_bf16 v[12:15], v[124:127], v[16:19], v[20:23]
	v_mfma_f32_16x16x32_bf16 v[20:23], v[128:131], v[16:19], v[24:27]
	v_mfma_f32_16x16x32_bf16 v[24:27], v[132:135], v[16:19], v[28:31]
	v_mfma_f32_16x16x32_bf16 v[8:11], v[136:139], v[16:19], v[8:11]
	v_mfma_f32_16x16x32_bf16 v[12:15], v[140:143], v[4:7], v[12:15]
	v_mfma_f32_16x16x32_bf16 v[16:19], v[144:147], v[4:7], v[20:23]
	v_mfma_f32_16x16x32_bf16 v[20:23], v[148:151], v[4:7], v[24:27]
	v_mfma_f32_16x16x32_bf16 v[4:7], v[152:155], v[4:7], v[8:11]
	v_mfma_f32_16x16x32_bf16 v[8:11], v[84:87], v[0:3], v[12:15]
	v_mfma_f32_16x16x32_bf16 v[12:15], v[156:159], v[0:3], v[16:19]
	v_mfma_f32_16x16x32_bf16 v[16:19], v[88:91], v[0:3], v[20:23]
	s_nop 5
	v_cvt_pk_bf16_f32 v8, v8, v9
	v_cvt_pk_bf16_f32 v9, v10, v11
	v_mfma_f32_16x16x32_bf16 v[4:7], v[160:163], v[0:3], v[4:7]
	v_lshl_add_u64 v[0:1], v[180:181], 0, s[34:35]
	global_store_dwordx2 v[0:1], v[8:9], off
	v_cvt_pk_bf16_f32 v8, v12, v13
	v_cvt_pk_bf16_f32 v9, v14, v15
	global_store_dwordx2 v[0:1], v[8:9], off offset:32
	v_cvt_pk_bf16_f32 v8, v16, v17
	v_cvt_pk_bf16_f32 v9, v18, v19
	s_nop 0
	v_cvt_pk_bf16_f32 v4, v4, v5
	v_cvt_pk_bf16_f32 v5, v6, v7
	global_store_dwordx2 v[0:1], v[8:9], off offset:64
	global_store_dwordx2 v[0:1], v[4:5], off offset:96
	s_cbranch_scc0 .LBB0_536

.LBB0_565:
	v_lshl_add_u64 v[190:191], v[204:205], 0, s[6:7]
	s_mov_b64 s[10:11], 0x1b0000
	v_lshl_add_u64 v[0:1], v[190:191], 0, s[10:11]
	s_add_i32 s9, s8, s18
	s_mov_b32 s10, m0
	s_mov_b32 m0, s9
	s_nop 0
	global_load_lds_dwordx4 v[0:1], off
	s_mov_b32 m0, s10
	v_add_u32_e32 v0, s29, v224
	ds_read_b128 v[186:189], v0 offset:4096
	ds_read_b128 v[230:233], v0 offset:4608
	ds_read_b128 v[234:237], v0 offset:6144
	ds_read_b128 v[238:241], v0 offset:6656
	s_lshl_b32 s8, s8, 1
	v_add_u32_e32 v3, s8, v225
	ds_read_b64_tr_b16 v[8:9], v3 offset:24576
	ds_read_b64_tr_b16 v[10:11], v3 offset:25088
	s_waitcnt lgkmcnt(9)
	v_mfma_f32_32x32x16_bf16 v[80:95], v[166:169], v[158:161], 0
	ds_read_b64_tr_b16 v[4:5], v3 offset:28672
	ds_read_b64_tr_b16 v[6:7], v3 offset:29184
	s_waitcnt lgkmcnt(10)
	v_mfma_f32_32x32x16_bf16 v[98:113], v[162:165], v[158:161], 0
	ds_read_b64_tr_b16 v[12:13], v3 offset:25600
	ds_read_b64_tr_b16 v[14:15], v3 offset:26112
	s_waitcnt lgkmcnt(11)
	v_mfma_f32_32x32x16_bf16 v[80:95], v[174:177], v[154:157], v[80:95]
	ds_read_b64_tr_b16 v[182:183], v3 offset:29696
	ds_read_b64_tr_b16 v[184:185], v3 offset:30208
	s_waitcnt lgkmcnt(12)
	v_mfma_f32_32x32x16_bf16 v[98:113], v[170:173], v[154:157], v[98:113]
	ds_read_b64_tr_b16 v[178:179], v3 offset:26624
	ds_read_b64_tr_b16 v[180:181], v3 offset:27136
	s_waitcnt lgkmcnt(13)
	v_mfma_f32_32x32x16_bf16 v[80:95], v[186:189], v[150:153], v[80:95]
	ds_read_b64_tr_b16 v[174:175], v3 offset:30720
	ds_read_b64_tr_b16 v[176:177], v3 offset:31232
	s_waitcnt lgkmcnt(14)
	v_mfma_f32_32x32x16_bf16 v[98:113], v[230:233], v[150:153], v[98:113]
	ds_read_b64_tr_b16 v[170:171], v3 offset:27648
	ds_read_b64_tr_b16 v[172:173], v3 offset:28160
	s_waitcnt lgkmcnt(14)
	v_mfma_f32_32x32x16_bf16 v[80:95], v[234:237], v[146:149], v[80:95]
	ds_read_b64_tr_b16 v[166:167], v3 offset:31744
	ds_read_b64_tr_b16 v[168:169], v3 offset:32256
	v_mfma_f32_32x32x16_bf16 v[98:113], v[238:241], v[146:149], v[98:113]
	v_lshl_add_u64 v[0:1], v[208:209], 0, s[6:7]
	s_mov_b64 s[8:9], 0x38121e00
	v_lshl_add_u64 v[96:97], v[0:1], 0, s[8:9]
	s_lshl_b32 s8, s24, 1
	s_mov_b64 s[10:11], 0x38121e80
	s_add_i32 s8, s8, s19
	s_mov_b32 s9, m0
	s_mov_b32 m0, s8
	s_nop 0
	global_load_lds_dwordx4 v[96:97], off
	s_mov_b32 m0, s9
	v_lshl_add_u64 v[96:97], v[0:1], 0, s[10:11]
	s_addk_i32 s8, 0x2000
	s_mov_b32 s9, m0
	s_mov_b32 m0, s8
	s_nop 0
	global_load_lds_dwordx4 v[96:97], off
	s_mov_b32 m0, s9
	s_nop 0
	v_pk_add_f32 v[96:97], v[80:81], v[206:207] op_sel_hi:[1,0] neg_lo:[0,1] neg_hi:[0,1]
	s_nop 1
	v_pk_add_f32 v[80:81], v[98:99], v[206:207] op_sel_hi:[1,0] neg_lo:[0,1] neg_hi:[0,1]
	v_pk_add_f32 v[98:99], v[82:83], v[206:207] op_sel_hi:[1,0] neg_lo:[0,1] neg_hi:[0,1]
	v_pk_add_f32 v[82:83], v[100:101], v[206:207] op_sel_hi:[1,0] neg_lo:[0,1] neg_hi:[0,1]
	v_pk_add_f32 v[100:101], v[84:85], v[206:207] op_sel_hi:[1,0] neg_lo:[0,1] neg_hi:[0,1]
	v_pk_add_f32 v[84:85], v[102:103], v[206:207] op_sel_hi:[1,0] neg_lo:[0,1] neg_hi:[0,1]
	v_pk_add_f32 v[102:103], v[86:87], v[206:207] op_sel_hi:[1,0] neg_lo:[0,1] neg_hi:[0,1]
	v_pk_add_f32 v[86:87], v[104:105], v[206:207] op_sel_hi:[1,0] neg_lo:[0,1] neg_hi:[0,1]
	v_pk_add_f32 v[104:105], v[88:89], v[206:207] op_sel_hi:[1,0] neg_lo:[0,1] neg_hi:[0,1]
	v_pk_add_f32 v[88:89], v[106:107], v[206:207] op_sel_hi:[1,0] neg_lo:[0,1] neg_hi:[0,1]
	v_pk_add_f32 v[106:107], v[90:91], v[206:207] op_sel_hi:[1,0] neg_lo:[0,1] neg_hi:[0,1]
	v_pk_add_f32 v[90:91], v[108:109], v[206:207] op_sel_hi:[1,0] neg_lo:[0,1] neg_hi:[0,1]
	v_pk_add_f32 v[108:109], v[92:93], v[206:207] op_sel_hi:[1,0] neg_lo:[0,1] neg_hi:[0,1]
	v_pk_add_f32 v[92:93], v[110:111], v[206:207] op_sel_hi:[1,0] neg_lo:[0,1] neg_hi:[0,1]
	v_pk_add_f32 v[110:111], v[94:95], v[206:207] op_sel_hi:[1,0] neg_lo:[0,1] neg_hi:[0,1]
	v_pk_add_f32 v[94:95], v[112:113], v[206:207] op_sel_hi:[1,0] neg_lo:[0,1] neg_hi:[0,1]
	v_max_f32_e32 v112, v96, v97
	v_max3_f32 v113, v98, v99, v81
	v_max3_f32 v112, v112, v80, v82
	v_max3_f32 v112, v112, v83, v100
	v_max3_f32 v113, v113, v102, v103
	v_max3_f32 v112, v112, v101, v84
	v_max3_f32 v113, v113, v86, v87
	v_max3_f32 v112, v112, v85, v104
	v_max3_f32 v113, v113, v106, v107
	v_max3_f32 v112, v112, v105, v88
	v_max3_f32 v113, v113, v90, v91
	v_max3_f32 v112, v112, v89, v108
	v_max3_f32 v113, v113, v110, v111
	v_max3_f32 v112, v112, v109, v92
	v_max3_f32 v113, v113, v94, v95
	v_max3_f32 v112, v112, v93, v113
	v_mov_b32_e32 v113, v112
	s_nop 1
	v_permlane32_swap_b32_e32 v112, v113
	v_max_f32_e32 v112, v112, v113
	s_mov_b32 s8, 0x41000000
	v_cmp_lt_f32_e32 vcc, s8, v112
	s_cmp_lg_u64 vcc, 0
	s_cselect_b64 s[8:9], -1, 0
	s_cbranch_vccnz .LBB0_573

.LBB0_568:
	s_add_i32 s8, s24, 0x2000
	s_cmpk_lg_i32 s24, 0x4000
	v_add_f32_e32 v3, v227, v3
	s_cselect_b32 s27, s8, 0
	s_mov_b64 s[8:9], 0x240000
	v_lshl_add_u64 v[80:81], v[190:191], 0, s[8:9]
	s_add_i32 s8, s29, s18
	s_mov_b32 s9, m0
	s_mov_b32 m0, s8
	s_nop 0
	global_load_lds_dwordx4 v[80:81], off
	s_mov_b32 m0, s9
	ds_read_b128 v[186:189], v192 offset:4096
	ds_read_b128 v[230:233], v192 offset:4608
	ds_read_b128 v[234:237], v192 offset:6144
	ds_read_b128 v[190:193], v192 offset:6656
	s_lshl_b32 s8, s29, 1
	v_add_u32_e32 v130, s8, v225
	ds_read_b64_tr_b16 v[174:175], v130 offset:24576
	ds_read_b64_tr_b16 v[176:177], v130 offset:25088
	v_mfma_f32_32x32x16_bf16 v[80:95], v[8:11], v[158:161], 0
	ds_read_b64_tr_b16 v[166:167], v130 offset:28672
	ds_read_b64_tr_b16 v[168:169], v130 offset:29184
	v_mfma_f32_32x32x16_bf16 v[98:113], v[4:7], v[158:161], 0
	ds_read_b64_tr_b16 v[170:171], v130 offset:25600
	ds_read_b64_tr_b16 v[172:173], v130 offset:26112
	v_mfma_f32_32x32x16_bf16 v[80:95], v[162:165], v[154:157], v[80:95]
	ds_read_b64_tr_b16 v[182:183], v130 offset:29696
	ds_read_b64_tr_b16 v[184:185], v130 offset:30208
	v_mfma_f32_32x32x16_bf16 v[98:113], v[12:15], v[154:157], v[98:113]
	ds_read_b64_tr_b16 v[178:179], v130 offset:26624
	ds_read_b64_tr_b16 v[180:181], v130 offset:27136
	s_waitcnt lgkmcnt(13)
	v_mfma_f32_32x32x16_bf16 v[80:95], v[186:189], v[150:153], v[80:95]
	ds_read_b64_tr_b16 v[12:13], v130 offset:30720
	ds_read_b64_tr_b16 v[14:15], v130 offset:31232
	s_waitcnt lgkmcnt(14)
	v_mfma_f32_32x32x16_bf16 v[98:113], v[230:233], v[150:153], v[98:113]
	ds_read_b64_tr_b16 v[8:9], v130 offset:27648
	ds_read_b64_tr_b16 v[10:11], v130 offset:28160
	s_waitcnt lgkmcnt(14)
	v_mfma_f32_32x32x16_bf16 v[80:95], v[234:237], v[146:149], v[80:95]
	ds_read_b64_tr_b16 v[4:5], v130 offset:31744
	ds_read_b64_tr_b16 v[6:7], v130 offset:32256
	v_mfma_f32_32x32x16_bf16 v[98:113], v[190:193], v[146:149], v[98:113]
	s_mov_b64 s[8:9], 0x381b1e00
	v_lshl_add_u64 v[96:97], v[0:1], 0, s[8:9]
	s_lshl_b32 s8, s27, 1
	s_add_i32 s10, s8, s19
	s_mov_b32 s8, m0
	s_mov_b32 m0, s10
	s_nop 0
	global_load_lds_dwordx4 v[96:97], off
	s_mov_b32 m0, s8
	s_mov_b64 s[8:9], 0x381b1e80
	v_lshl_add_u64 v[0:1], v[0:1], 0, s[8:9]
	s_nop 2
	v_pk_add_f32 v[80:81], v[80:81], v[206:207] op_sel_hi:[1,0] neg_lo:[0,1] neg_hi:[0,1]
	s_add_i32 s8, s10, 0x2000
	s_mov_b32 s9, m0
	s_mov_b32 m0, s8
	s_nop 0
	global_load_lds_dwordx4 v[0:1], off
	s_mov_b32 m0, s9
	s_nop 0
	v_pk_add_f32 v[0:1], v[98:99], v[206:207] op_sel_hi:[1,0] neg_lo:[0,1] neg_hi:[0,1]
	v_pk_add_f32 v[98:99], v[82:83], v[206:207] op_sel_hi:[1,0] neg_lo:[0,1] neg_hi:[0,1]
	v_pk_add_f32 v[82:83], v[100:101], v[206:207] op_sel_hi:[1,0] neg_lo:[0,1] neg_hi:[0,1]
	v_max_f32_e32 v96, v80, v81
	v_pk_add_f32 v[100:101], v[84:85], v[206:207] op_sel_hi:[1,0] neg_lo:[0,1] neg_hi:[0,1]
	v_pk_add_f32 v[84:85], v[102:103], v[206:207] op_sel_hi:[1,0] neg_lo:[0,1] neg_hi:[0,1]
	v_pk_add_f32 v[102:103], v[86:87], v[206:207] op_sel_hi:[1,0] neg_lo:[0,1] neg_hi:[0,1]
	v_max3_f32 v97, v98, v99, v1
	v_max3_f32 v96, v96, v0, v82
	v_pk_add_f32 v[86:87], v[104:105], v[206:207] op_sel_hi:[1,0] neg_lo:[0,1] neg_hi:[0,1]
	v_max3_f32 v96, v96, v83, v100
	v_max3_f32 v97, v97, v102, v103
	v_pk_add_f32 v[104:105], v[88:89], v[206:207] op_sel_hi:[1,0] neg_lo:[0,1] neg_hi:[0,1]
	v_pk_add_f32 v[88:89], v[106:107], v[206:207] op_sel_hi:[1,0] neg_lo:[0,1] neg_hi:[0,1]
	v_pk_add_f32 v[106:107], v[90:91], v[206:207] op_sel_hi:[1,0] neg_lo:[0,1] neg_hi:[0,1]
	v_max3_f32 v96, v96, v101, v84
	v_max3_f32 v97, v97, v86, v87
	v_pk_add_f32 v[90:91], v[108:109], v[206:207] op_sel_hi:[1,0] neg_lo:[0,1] neg_hi:[0,1]
	v_max3_f32 v96, v96, v85, v104
	v_max3_f32 v97, v97, v106, v107
	v_pk_add_f32 v[108:109], v[92:93], v[206:207] op_sel_hi:[1,0] neg_lo:[0,1] neg_hi:[0,1]
	v_pk_add_f32 v[92:93], v[110:111], v[206:207] op_sel_hi:[1,0] neg_lo:[0,1] neg_hi:[0,1]
	v_pk_add_f32 v[110:111], v[94:95], v[206:207] op_sel_hi:[1,0] neg_lo:[0,1] neg_hi:[0,1]
	v_max3_f32 v96, v96, v105, v88
	v_max3_f32 v97, v97, v90, v91
	v_pk_add_f32 v[94:95], v[112:113], v[206:207] op_sel_hi:[1,0] neg_lo:[0,1] neg_hi:[0,1]
	v_max3_f32 v96, v96, v89, v108
	v_max3_f32 v97, v97, v110, v111
	v_max3_f32 v96, v96, v109, v92
	v_max3_f32 v97, v97, v94, v95
	v_max3_f32 v96, v96, v93, v97
	v_mov_b32_e32 v97, v96
	s_nop 1
	v_permlane32_swap_b32_e32 v96, v97
	v_max_f32_e32 v96, v96, v97
	s_mov_b32 s8, 0x41000000
	v_cmp_lt_f32_e32 vcc, s8, v96
	s_cmp_lg_u64 vcc, 0
	s_cselect_b64 s[8:9], -1, 0
	s_cbranch_vccnz .LBB0_576

; __device__ __forceinline__ void cmask(f32x16&p0,f32x16&p1,int jb,int qrel,int hi){
;   const float NEG=-INFINITY; int kb=64*jb+4*hi;
;   #pragma unroll
;   for(int r=0;r<16;++r){int kv=kb+(r&3)+8*(r>>2); if(kv>qrel)p0[r]=NEG; if(kv+32>qrel)p1[r]=NEG;}
; }
.LBB0_582:
	v_add_u32_e32 v0, s25, v224
	ds_read_b128 v[4:7], v0 offset:4096
	ds_read_b128 v[8:11], v0 offset:4608
	ds_read_b128 v[182:185], v0 offset:6144
	ds_read_b128 v[186:189], v0 offset:6656
	v_add_u32_e32 v0, s28, v225
	ds_read_b64_tr_b16 v[178:179], v0 offset:24576
	ds_read_b64_tr_b16 v[180:181], v0 offset:25088
	s_waitcnt lgkmcnt(9)
	v_mfma_f32_32x32x16_bf16 v[96:111], v[166:169], v[158:161], 0
	ds_read_b64_tr_b16 v[166:167], v0 offset:28672
	ds_read_b64_tr_b16 v[168:169], v0 offset:29184
	s_waitcnt lgkmcnt(10)
	v_mfma_f32_32x32x16_bf16 v[80:95], v[162:165], v[158:161], 0
	ds_read_b64_tr_b16 v[162:163], v0 offset:25600
	ds_read_b64_tr_b16 v[164:165], v0 offset:26112
	s_waitcnt lgkmcnt(11)
	v_mfma_f32_32x32x16_bf16 v[96:111], v[174:177], v[154:157], v[96:111]
	ds_read_b64_tr_b16 v[158:159], v0 offset:29696
	ds_read_b64_tr_b16 v[160:161], v0 offset:30208
	s_waitcnt lgkmcnt(12)
	v_mfma_f32_32x32x16_bf16 v[80:95], v[170:173], v[154:157], v[80:95]
	ds_read_b64_tr_b16 v[112:113], v0 offset:26624
	ds_read_b64_tr_b16 v[114:115], v0 offset:27136
	s_waitcnt lgkmcnt(13)
	v_mfma_f32_32x32x16_bf16 v[96:111], v[4:7], v[150:153], v[96:111]
	ds_read_b64_tr_b16 v[12:13], v0 offset:30720
	ds_read_b64_tr_b16 v[14:15], v0 offset:31232
	s_waitcnt lgkmcnt(14)
	v_mfma_f32_32x32x16_bf16 v[80:95], v[8:11], v[150:153], v[80:95]
	ds_read_b64_tr_b16 v[8:9], v0 offset:27648
	ds_read_b64_tr_b16 v[10:11], v0 offset:28160
	s_waitcnt lgkmcnt(14)
	v_mfma_f32_32x32x16_bf16 v[96:111], v[182:185], v[146:149], v[96:111]
	ds_read_b64_tr_b16 v[4:5], v0 offset:31744
	ds_read_b64_tr_b16 v[6:7], v0 offset:32256
	v_mfma_f32_32x32x16_bf16 v[80:95], v[186:189], v[146:149], v[80:95]
	s_nop 8
	v_sub_f32_e32 v1, v111, v206
	v_or_b32_e32 v111, 0xe0, v220
	v_sub_f32_e32 v3, v110, v206
	v_sub_f32_e32 v80, v80, v206
	v_or_b32_e32 v110, 0xc0, v220
	v_cmp_le_i32_e32 vcc, v111, v223
	v_sub_f32_e32 v97, v97, v206
	v_sub_f32_e32 v96, v96, v206
	v_cndmask_b32_e32 v80, v216, v80, vcc
	v_cmp_lt_i32_e32 vcc, v110, v223
	v_sub_f32_e32 v81, v81, v206
	v_sub_f32_e32 v98, v98, v206
	v_cndmask_b32_e32 v97, v216, v97, vcc
	v_cmp_le_i32_e32 vcc, v110, v223
	v_or_b32_e32 v110, 0xe1, v220
	v_sub_f32_e32 v82, v82, v206
	v_cndmask_b32_e32 v96, v216, v96, vcc
	v_cmp_le_i32_e32 vcc, v110, v223
	v_or_b32_e32 v110, 0xc2, v220
	v_sub_f32_e32 v99, v99, v206
	v_cndmask_b32_e32 v81, v216, v81, vcc
	v_cmp_le_i32_e32 vcc, v110, v223
	v_or_b32_e32 v110, 0xe2, v220
	v_sub_f32_e32 v83, v83, v206
	v_cndmask_b32_e32 v98, v216, v98, vcc
	v_cmp_le_i32_e32 vcc, v110, v223
	v_or_b32_e32 v110, 0xc3, v220
	v_sub_f32_e32 v100, v100, v206
	v_cndmask_b32_e32 v82, v216, v82, vcc
	v_cmp_le_i32_e32 vcc, v110, v223
	v_or_b32_e32 v110, 0xe3, v220
	v_sub_f32_e32 v84, v84, v206
	v_cndmask_b32_e32 v99, v216, v99, vcc
	v_cmp_le_i32_e32 vcc, v110, v223
	v_or_b32_e32 v110, 0xc8, v220
	v_sub_f32_e32 v101, v101, v206
	v_cndmask_b32_e32 v83, v216, v83, vcc
	v_cmp_le_i32_e32 vcc, v110, v223
	v_or_b32_e32 v110, 0xe8, v220
	v_sub_f32_e32 v85, v85, v206
	v_cndmask_b32_e32 v100, v216, v100, vcc
	v_cmp_le_i32_e32 vcc, v110, v223
	v_or_b32_e32 v110, 0xc9, v220
	v_sub_f32_e32 v102, v102, v206
	v_cndmask_b32_e32 v84, v216, v84, vcc
	v_cmp_le_i32_e32 vcc, v110, v223
	v_or_b32_e32 v110, 0xe9, v220
	v_sub_f32_e32 v86, v86, v206
	v_cndmask_b32_e32 v101, v216, v101, vcc
	v_cmp_le_i32_e32 vcc, v110, v223
	v_or_b32_e32 v110, 0xca, v220
	v_sub_f32_e32 v103, v103, v206
	v_cndmask_b32_e32 v85, v216, v85, vcc
	v_cmp_le_i32_e32 vcc, v110, v223
	v_or_b32_e32 v110, 0xea, v220
	v_sub_f32_e32 v87, v87, v206
	v_cndmask_b32_e32 v102, v216, v102, vcc
	v_cmp_le_i32_e32 vcc, v110, v223
	v_or_b32_e32 v110, 0xcb, v220
	v_sub_f32_e32 v104, v104, v206
	v_cndmask_b32_e32 v86, v216, v86, vcc
	v_cmp_le_i32_e32 vcc, v110, v223
	v_or_b32_e32 v110, 0xeb, v220
	v_sub_f32_e32 v88, v88, v206
	v_cndmask_b32_e32 v103, v216, v103, vcc
	v_cmp_le_i32_e32 vcc, v110, v223
	v_or_b32_e32 v110, 0xd0, v220
	v_sub_f32_e32 v105, v105, v206
	v_cndmask_b32_e32 v87, v216, v87, vcc
	v_cmp_le_i32_e32 vcc, v110, v223
	v_or_b32_e32 v110, 0xf0, v220
	v_sub_f32_e32 v89, v89, v206
	v_cndmask_b32_e32 v104, v216, v104, vcc
	v_cmp_le_i32_e32 vcc, v110, v223
	v_or_b32_e32 v110, 0xd1, v220
	v_sub_f32_e32 v106, v106, v206
	v_cndmask_b32_e32 v88, v216, v88, vcc
	v_cmp_le_i32_e32 vcc, v110, v223
	v_or_b32_e32 v110, 0xf1, v220
	v_sub_f32_e32 v90, v90, v206
	v_cndmask_b32_e32 v105, v216, v105, vcc
	v_cmp_le_i32_e32 vcc, v110, v223
	v_or_b32_e32 v110, 0xd2, v220
	v_sub_f32_e32 v107, v107, v206
	v_cndmask_b32_e32 v89, v216, v89, vcc
	v_cmp_le_i32_e32 vcc, v110, v223
	v_or_b32_e32 v110, 0xf2, v220
	v_sub_f32_e32 v91, v91, v206
	v_cndmask_b32_e32 v106, v216, v106, vcc
	v_cmp_le_i32_e32 vcc, v110, v223
	v_or_b32_e32 v110, 0xd3, v220
	v_sub_f32_e32 v108, v108, v206
	v_cndmask_b32_e32 v90, v216, v90, vcc
	v_cmp_le_i32_e32 vcc, v110, v223
	v_or_b32_e32 v110, 0xf3, v220
	v_sub_f32_e32 v92, v92, v206
	v_cndmask_b32_e32 v107, v216, v107, vcc
	v_cmp_le_i32_e32 vcc, v110, v223
	v_or_b32_e32 v110, 0xd8, v220
	v_sub_f32_e32 v109, v109, v206
	v_cndmask_b32_e32 v91, v216, v91, vcc
	v_cmp_le_i32_e32 vcc, v110, v223
	v_or_b32_e32 v110, 0xf8, v220
	v_sub_f32_e32 v93, v93, v206
	v_cndmask_b32_e32 v108, v216, v108, vcc
	v_cmp_le_i32_e32 vcc, v110, v223
	v_or_b32_e32 v110, 0xd9, v220
	v_sub_f32_e32 v94, v94, v206
	v_cndmask_b32_e32 v92, v216, v92, vcc
	v_cmp_le_i32_e32 vcc, v110, v223
	v_or_b32_e32 v110, 0xf9, v220
	v_sub_f32_e32 v95, v95, v206
	v_cndmask_b32_e32 v109, v216, v109, vcc
	v_cmp_le_i32_e32 vcc, v110, v223
	v_or_b32_e32 v110, 0xda, v220
	s_mov_b32 s0, 0x41000000
	v_cndmask_b32_e32 v93, v216, v93, vcc
	v_cmp_le_i32_e32 vcc, v110, v223
	s_nop 1
	v_cndmask_b32_e32 v110, v216, v3, vcc
	v_or_b32_e32 v3, 0xfa, v220
	v_cmp_le_i32_e32 vcc, v3, v223
	v_or_b32_e32 v3, 0xdb, v220
	s_nop 0
	v_cndmask_b32_e32 v94, v216, v94, vcc
	v_cmp_le_i32_e32 vcc, v3, v223
	v_max3_f32 v3, v98, v99, v81
	v_max3_f32 v3, v3, v102, v103
	v_cndmask_b32_e32 v111, v216, v1, vcc
	v_or_b32_e32 v1, 0xfb, v220
	v_cmp_le_i32_e32 vcc, v1, v223
	v_max_f32_e32 v1, v96, v97
	v_max3_f32 v1, v1, v80, v82
	v_max3_f32 v1, v1, v83, v100
	v_max3_f32 v1, v1, v101, v84
	v_max3_f32 v3, v3, v86, v87
	v_max3_f32 v1, v1, v85, v104
	v_max3_f32 v3, v3, v106, v107
	v_max3_f32 v1, v1, v105, v88
	v_max3_f32 v3, v3, v90, v91
	v_cndmask_b32_e32 v95, v216, v95, vcc
	v_max3_f32 v1, v1, v89, v108
	v_max3_f32 v3, v3, v110, v111
	v_max3_f32 v1, v1, v109, v92
	v_max3_f32 v3, v3, v94, v95
	v_max3_f32 v1, v1, v93, v3
	v_mov_b32_e32 v3, v1
	s_nop 1
	v_permlane32_swap_b32_e32 v1, v3
	v_max_f32_e32 v1, v1, v3
	v_cmp_lt_f32_e32 vcc, s0, v1
	s_cmp_lg_u64 vcc, 0
	s_cselect_b64 s[0:1], -1, 0
	s_cbranch_vccnz .LBB0_626

.LBB0_594:
	v_max_f32_e32 v119, v97, v97
	v_max_f32_e32 v122, v96, v96
	v_max_f32_e32 v119, v122, v119
	v_max3_f32 v122, v98, v99, v81
	v_max3_f32 v119, v119, v80, v82
	v_max3_f32 v119, v119, v83, v100
	v_max3_f32 v122, v122, v102, v103
	v_max3_f32 v119, v119, v101, v84
	v_max3_f32 v122, v122, v86, v87
	v_max3_f32 v119, v119, v85, v104
	v_max3_f32 v122, v122, v106, v107
	v_max3_f32 v119, v119, v105, v88
	v_max3_f32 v122, v122, v90, v91
	v_max3_f32 v119, v119, v89, v108
	v_max3_f32 v122, v122, v110, v111
	v_max3_f32 v119, v119, v109, v92
	v_max3_f32 v122, v122, v94, v95
	v_max3_f32 v119, v119, v93, v122
	v_mov_b32_e32 v122, v119
	s_nop 1
	v_permlane32_swap_b32_e32 v119, v122
	v_max_f32_e32 v119, v119, v122
	s_mov_b32 s8, 0x41000000
	v_cmp_lt_f32_e32 vcc, s8, v119
	s_cmp_lg_u64 vcc, 0
	s_cselect_b64 s[8:9], -1, 0
	s_cbranch_vccnz .LBB0_620

.LBB0_605:
	v_max_f32_e32 v131, v97, v97
	v_max_f32_e32 v134, v96, v96
	v_max_f32_e32 v131, v134, v131
	v_max3_f32 v134, v98, v99, v81
	v_max3_f32 v131, v131, v80, v82
	v_max3_f32 v131, v131, v83, v100
	v_max3_f32 v134, v134, v102, v103
	v_max3_f32 v131, v131, v101, v84
	v_max3_f32 v134, v134, v86, v87
	v_max3_f32 v131, v131, v85, v104
	v_max3_f32 v134, v134, v106, v107
	v_max3_f32 v131, v131, v105, v88
	v_max3_f32 v134, v134, v90, v91
	v_max3_f32 v131, v131, v89, v108
	v_max3_f32 v134, v134, v110, v111
	v_max3_f32 v131, v131, v109, v92
	v_max3_f32 v134, v134, v94, v95
	v_max3_f32 v131, v131, v93, v134
	v_mov_b32_e32 v134, v131
	s_nop 1
	v_permlane32_swap_b32_e32 v131, v134
	v_max_f32_e32 v131, v131, v134
	s_mov_b32 s0, 0x41000000
	v_cmp_lt_f32_e32 vcc, s0, v131
	s_cmp_lg_u64 vcc, 0
	v_add_f32_e32 v113, v227, v113
	s_cselect_b64 s[0:1], -1, 0
	s_cbranch_vccnz .LBB0_623
